# v5 + GEMM main loops: the barrier before each MFMA block moved 8 MFMAs into the block (matrix pipe busy during the barrier handshake)
# speedup vs baseline: 1.0004x; 1.0004x over previous
; #define PG8_STAGE(bufoff, gbase, voff) do { _Pragma("unroll") for (int _i = 0; _i < 2; ++_i) \
;         __builtin_amdgcn_global_load_lds((const unsigned*)((const char*)(gbase) + (voff)[_i]), (PG8_LAS unsigned*)(lds + (bufoff) + ldsw + _i * 8192), 16, 0, 0); } while (0)
; #define PG8_LDA(dst, b, h) do { _Pragma("unroll") for (int m = 0; m < 4; ++m) _Pragma("unroll") for (int k = 0; k < 2; ++k) dst[m][k] = *(const PG8_LAS bf16x8*)(lds + PG8_SA(b, h) + aoff + m * 2048 + k * 1024); } while (0)
; #define PG8_LDB(dst, b, h) do { _Pragma("unroll") for (int n = 0; n < 2; ++n) _Pragma("unroll") for (int k = 0; k < 2; ++k) dst[n][k] = *(const PG8_LAS bf16x8*)(lds + PG8_SB(b, h) + boff + n * 2048 + k * 1024); } while (0)
; #define PG8_MMA(ai, bj, At, Bt) do { __builtin_amdgcn_s_setprio(1); _Pragma("unroll") for (int m = 0; m < 4; ++m) _Pragma("unroll") for (int n = 0; n < 2; ++n) _Pragma("unroll") for (int k = 0; k < 2; ++k) \
;         acc[ai][bj][m][n] = mma16<I8>(Bt[n][k], At[m][k], acc[ai][bj][m][n]); __builtin_amdgcn_s_setprio(0); } while (0)
; #define PG8_WAIT_V(n) asm volatile("s_waitcnt vmcnt(" #n ")" ::: "memory")
; #define PG8_WAIT_L(n) asm volatile("s_waitcnt lgkmcnt(" #n ")" ::: "memory")
; #define PG8_BAR __builtin_amdgcn_s_barrier()
; #define PG8_SCHED __builtin_amdgcn_sched_barrier(0)
; template <class Epi, class Sched, bool ALIGN_EPI = false, bool SP2 = false, bool I8 = false>
; __device__ __forceinline__ void gemm_phase(PG8_LAS unsigned char* lds, const Gemm g, const Sched& S, const Epi& E) {
;     ...
;             PG8_LDB(B0, 0, 0); PG8_LDB(B1, 0, 1); PG8_SCHED; PG8_LDA(At, 0, 0); PG8_STAGE(PG8_SA(1, 1), a1 + hstep, voffA);
;             PG8_WAIT_V(8); PG8_WAIT_L(0); PG8_BAR; PG8_MMA(0, 0, At, B0); PG8_MMA(0, 1, At, B1); PG8_BAR; PG8_SCHED;
;             PG8_LDA(At, 0, 1); PG8_STAGE(PG8_SB(0, 0), b2, voffB); PG8_STAGE(PG8_SB(0, 1), b2 + hstep, voffB); PG8_STAGE(PG8_SA(0, 0), a2, voffA);
;             PG8_WAIT_V(8); PG8_WAIT_L(0); PG8_BAR; PG8_MMA(1, 0, At, B0); PG8_MMA(1, 1, At, B1); PG8_BAR; PG8_SCHED;
.LBB0_276:
	ds_read_b128 v[22:25], v203
	ds_read_b128 v[30:33], v203 offset:1024
	ds_read_b128 v[34:37], v203 offset:2048
	ds_read_b128 v[38:41], v203 offset:3072
	ds_read_b128 v[168:171], v204
	ds_read_b128 v[172:175], v204 offset:1024
	ds_read_b128 v[176:179], v204 offset:2048
	ds_read_b128 v[180:183], v204 offset:3072
	s_add_u32 s47, s42, 0xfffc0080
	s_addc_u32 s48, s43, -1
	s_cmp_eq_u32 s46, 12
	s_cselect_b32 s69, s5, s48
	s_cselect_b32 s68, s33, s47
	s_cselect_b32 s63, s35, s45
	s_cselect_b32 s62, s37, s44
	v_lshl_add_u64 v[226:227], s[42:43], 0, v[160:161]
	s_add_i32 m0, s3, 0xc000
	ds_read_b128 v[184:187], v205
	ds_read_b128 v[188:191], v205 offset:1024
	ds_read_b128 v[192:195], v205 offset:2048
	ds_read_b128 v[206:209], v205 offset:3072
	ds_read_b128 v[210:213], v205 offset:4096
	ds_read_b128 v[214:217], v205 offset:5120
	ds_read_b128 v[218:221], v205 offset:6144
	ds_read_b128 v[222:225], v205 offset:7168
	global_load_lds_dwordx4 v[226:227], off
	v_lshl_add_u64 v[226:227], s[42:43], 0, v[162:163]
	s_add_i32 m0, s3, 0xe000
	s_nop 0
	global_load_lds_dwordx4 v[226:227], off
	s_waitcnt vmcnt(8)
	s_waitcnt lgkmcnt(0)
	s_setprio 1
	s_waitcnt lgkmcnt(0)
	v_mfma_i32_16x16x64_i8 v[142:145], v[22:25], v[184:187], v[142:145]
	v_mfma_i32_16x16x64_i8 v[138:141], v[34:37], v[184:187], v[138:141]
	v_mfma_i32_16x16x64_i8 v[126:129], v[22:25], v[192:195], v[126:129]
	v_mfma_i32_16x16x64_i8 v[122:125], v[34:37], v[192:195], v[122:125]
	v_mfma_i32_16x16x64_i8 v[110:113], v[22:25], v[210:213], v[110:113]
	v_mfma_i32_16x16x64_i8 v[106:109], v[34:37], v[210:213], v[106:109]
	v_mfma_i32_16x16x64_i8 v[94:97], v[22:25], v[218:221], v[94:97]
	v_mfma_i32_16x16x64_i8 v[90:93], v[34:37], v[218:221], v[90:93]
	s_barrier
	v_mfma_i32_16x16x64_i8 v[142:145], v[30:33], v[188:191], v[142:145]
	v_mfma_i32_16x16x64_i8 v[138:141], v[38:41], v[188:191], v[138:141]
	v_mfma_i32_16x16x64_i8 v[126:129], v[30:33], v[206:209], v[126:129]
	v_mfma_i32_16x16x64_i8 v[122:125], v[38:41], v[206:209], v[122:125]
	v_mfma_i32_16x16x64_i8 v[110:113], v[30:33], v[214:217], v[110:113]
	v_mfma_i32_16x16x64_i8 v[106:109], v[38:41], v[214:217], v[106:109]
	v_mfma_i32_16x16x64_i8 v[94:97], v[30:33], v[222:225], v[94:97]
	v_mfma_i32_16x16x64_i8 v[90:93], v[38:41], v[222:225], v[90:93]
	s_setprio 0
	s_setprio 1
	v_mfma_i32_16x16x64_i8 v[134:137], v[168:171], v[184:187], v[134:137]
	v_mfma_i32_16x16x64_i8 v[130:133], v[176:179], v[184:187], v[130:133]
	v_mfma_i32_16x16x64_i8 v[118:121], v[168:171], v[192:195], v[118:121]
	v_mfma_i32_16x16x64_i8 v[114:117], v[176:179], v[192:195], v[114:117]
	v_mfma_i32_16x16x64_i8 v[102:105], v[168:171], v[210:213], v[102:105]
	v_mfma_i32_16x16x64_i8 v[98:101], v[176:179], v[210:213], v[98:101]
	v_mfma_i32_16x16x64_i8 v[86:89], v[168:171], v[218:221], v[86:89]
	v_mfma_i32_16x16x64_i8 v[82:85], v[176:179], v[218:221], v[82:85]
	v_mfma_i32_16x16x64_i8 v[134:137], v[172:175], v[188:191], v[134:137]
	v_mfma_i32_16x16x64_i8 v[130:133], v[180:183], v[188:191], v[130:133]
	v_mfma_i32_16x16x64_i8 v[118:121], v[172:175], v[206:209], v[118:121]
	v_mfma_i32_16x16x64_i8 v[114:117], v[180:183], v[206:209], v[114:117]
	v_mfma_i32_16x16x64_i8 v[102:105], v[172:175], v[214:217], v[102:105]
	v_mfma_i32_16x16x64_i8 v[98:101], v[180:183], v[214:217], v[98:101]
	v_mfma_i32_16x16x64_i8 v[86:89], v[172:175], v[222:225], v[86:89]
	v_mfma_i32_16x16x64_i8 v[82:85], v[180:183], v[222:225], v[82:85]
	s_setprio 0
	s_barrier
	s_add_i32 s47, s84, s19
	v_lshl_add_u64 v[226:227], s[62:63], 0, v[154:155]
	s_mov_b32 m0, s47
	ds_read_b128 v[184:187], v205 offset:16384
	ds_read_b128 v[188:191], v205 offset:17408
	ds_read_b128 v[192:195], v205 offset:18432
	ds_read_b128 v[206:209], v205 offset:19456
	ds_read_b128 v[210:213], v205 offset:20480
	ds_read_b128 v[214:217], v205 offset:21504
	ds_read_b128 v[218:221], v205 offset:22528
	ds_read_b128 v[222:225], v205 offset:23552
	global_load_lds_dwordx4 v[226:227], off
	s_add_i32 m0, s47, 0x2000
	s_add_u32 s48, s62, 0x40000
	v_lshl_add_u64 v[228:229], s[62:63], 0, v[158:159]
	s_addc_u32 s49, s63, 0
	s_add_i32 s47, s85, s19
	global_load_lds_dwordx4 v[228:229], off
	v_lshl_add_u64 v[230:231], s[48:49], 0, v[154:155]
	s_mov_b32 m0, s47
	v_lshl_add_u64 v[232:233], s[68:69], 0, v[156:157]
	global_load_lds_dwordx4 v[230:231], off
	v_lshl_add_u64 v[230:231], s[48:49], 0, v[158:159]
	s_add_i32 m0, s47, 0x2000
	s_nop 0
	global_load_lds_dwordx4 v[230:231], off
	v_lshl_add_u64 v[230:231], s[68:69], 0, v[152:153]
	s_mov_b32 m0, s3
	s_nop 0
	global_load_lds_dwordx4 v[230:231], off
	s_mov_b32 m0, s21
	s_nop 0
	global_load_lds_dwordx4 v[232:233], off
	s_waitcnt vmcnt(8)
	s_waitcnt lgkmcnt(0)
	s_setprio 1
	s_waitcnt lgkmcnt(0)
	v_mfma_i32_16x16x64_i8 v[78:81], v[22:25], v[184:187], v[78:81]
	v_mfma_i32_16x16x64_i8 v[74:77], v[34:37], v[184:187], v[74:77]
	v_mfma_i32_16x16x64_i8 v[62:65], v[22:25], v[192:195], v[62:65]
	v_mfma_i32_16x16x64_i8 v[58:61], v[34:37], v[192:195], v[58:61]
	v_mfma_i32_16x16x64_i8 v[46:49], v[22:25], v[210:213], v[46:49]
	v_mfma_i32_16x16x64_i8 v[42:45], v[34:37], v[210:213], v[42:45]
	v_mfma_i32_16x16x64_i8 v[14:17], v[22:25], v[218:221], v[14:17]
	v_mfma_i32_16x16x64_i8 v[10:13], v[34:37], v[218:221], v[10:13]
	s_barrier
; #define PG8_STAGE(bufoff, gbase, voff) do { _Pragma("unroll") for (int _i = 0; _i < 2; ++_i) \
;         __builtin_amdgcn_global_load_lds((const unsigned*)((const char*)(gbase) + (voff)[_i]), (PG8_LAS unsigned*)(lds + (bufoff) + ldsw + _i * 8192), 16, 0, 0); } while (0)
; #define PG8_LDA(dst, b, h) do { _Pragma("unroll") for (int m = 0; m < 4; ++m) _Pragma("unroll") for (int k = 0; k < 2; ++k) dst[m][k] = *(const PG8_LAS bf16x8*)(lds + PG8_SA(b, h) + aoff + m * 2048 + k * 1024); } while (0)
; #define PG8_LDB(dst, b, h) do { _Pragma("unroll") for (int n = 0; n < 2; ++n) _Pragma("unroll") for (int k = 0; k < 2; ++k) dst[n][k] = *(const PG8_LAS bf16x8*)(lds + PG8_SB(b, h) + boff + n * 2048 + k * 1024); } while (0)
; #define PG8_MMA(ai, bj, At, Bt) do { __builtin_amdgcn_s_setprio(1); _Pragma("unroll") for (int m = 0; m < 4; ++m) _Pragma("unroll") for (int n = 0; n < 2; ++n) _Pragma("unroll") for (int k = 0; k < 2; ++k) \
;         acc[ai][bj][m][n] = mma16<I8>(Bt[n][k], At[m][k], acc[ai][bj][m][n]); __builtin_amdgcn_s_setprio(0); } while (0)
; #define PG8_WAIT_V(n) asm volatile("s_waitcnt vmcnt(" #n ")" ::: "memory")
; #define PG8_WAIT_L(n) asm volatile("s_waitcnt lgkmcnt(" #n ")" ::: "memory")
; #define PG8_BAR __builtin_amdgcn_s_barrier()
; #define PG8_SCHED __builtin_amdgcn_sched_barrier(0)
; template <class Epi, class Sched, bool ALIGN_EPI = false, bool SP2 = false, bool I8 = false>
; __device__ __forceinline__ void gemm_phase(PG8_LAS unsigned char* lds, const Gemm g, const Sched& S, const Epi& E) {
;     ...
;             PG8_WAIT_V(8); PG8_WAIT_L(0); PG8_BAR; PG8_MMA(1, 0, At, B0); PG8_MMA(1, 1, At, B1); PG8_BAR; PG8_SCHED;
;             PG8_LDB(B0, 1, 0); PG8_LDB(B1, 1, 1); PG8_SCHED; PG8_LDA(At, 1, 0); PG8_STAGE(PG8_SA(0, 1), a2 + hstep, voffA);
;             PG8_WAIT_V(8); PG8_WAIT_L(0); PG8_BAR; PG8_MMA(0, 0, At, B0); PG8_MMA(0, 1, At, B1); PG8_BAR; PG8_SCHED;
	v_mfma_i32_16x16x64_i8 v[78:81], v[30:33], v[188:191], v[78:81]
	v_mfma_i32_16x16x64_i8 v[74:77], v[38:41], v[188:191], v[74:77]
	v_mfma_i32_16x16x64_i8 v[62:65], v[30:33], v[206:209], v[62:65]
	v_mfma_i32_16x16x64_i8 v[58:61], v[38:41], v[206:209], v[58:61]
	v_mfma_i32_16x16x64_i8 v[46:49], v[30:33], v[214:217], v[46:49]
	v_mfma_i32_16x16x64_i8 v[42:45], v[38:41], v[214:217], v[42:45]
	v_mfma_i32_16x16x64_i8 v[14:17], v[30:33], v[222:225], v[14:17]
	v_mfma_i32_16x16x64_i8 v[10:13], v[38:41], v[222:225], v[10:13]
	s_setprio 0
	s_setprio 1
	v_mfma_i32_16x16x64_i8 v[26:29], v[168:171], v[210:213], v[26:29]
	v_mfma_i32_16x16x64_i8 v[18:21], v[176:179], v[210:213], v[18:21]
	v_mfma_i32_16x16x64_i8 v[6:9], v[168:171], v[218:221], v[6:9]
	v_mfma_i32_16x16x64_i8 v[2:5], v[176:179], v[218:221], v[2:5]
	v_mfma_i32_16x16x64_i8 v[22:25], v[168:171], v[184:187], v[70:73]
	v_mfma_i32_16x16x64_i8 v[30:33], v[176:179], v[184:187], v[66:69]
	v_mfma_i32_16x16x64_i8 v[34:37], v[168:171], v[192:195], v[54:57]
	v_mfma_i32_16x16x64_i8 v[38:41], v[176:179], v[192:195], v[50:53]
	v_mfma_i32_16x16x64_i8 v[26:29], v[172:175], v[214:217], v[26:29]
	v_mfma_i32_16x16x64_i8 v[18:21], v[180:183], v[214:217], v[18:21]
	v_mfma_i32_16x16x64_i8 v[6:9], v[172:175], v[222:225], v[6:9]
	v_mfma_i32_16x16x64_i8 v[2:5], v[180:183], v[222:225], v[2:5]
	v_mfma_i32_16x16x64_i8 v[22:25], v[172:175], v[188:191], v[22:25]
	v_mfma_i32_16x16x64_i8 v[30:33], v[180:183], v[188:191], v[30:33]
	v_mfma_i32_16x16x64_i8 v[34:37], v[172:175], v[206:209], v[34:37]
	v_mfma_i32_16x16x64_i8 v[38:41], v[180:183], v[206:209], v[38:41]
	s_setprio 0
	s_barrier
	s_add_i32 s47, 0, 0x18000
	s_add_i32 s50, 0, 0x1c000
	v_add_u32_e32 v70, s47, v201
	v_add_u32_e32 v180, s50, v201
	ds_read_b128 v[50:53], v70
	ds_read_b128 v[54:57], v70 offset:1024
	ds_read_b128 v[66:69], v70 offset:2048
	ds_read_b128 v[70:73], v70 offset:3072
	ds_read_b128 v[168:171], v180
	ds_read_b128 v[172:175], v180 offset:1024
	ds_read_b128 v[176:179], v180 offset:2048
	ds_read_b128 v[180:183], v180 offset:3072
	s_add_u32 s48, s68, 0x40000
	s_addc_u32 s49, s69, 0
	s_mov_b32 m0, s23
	v_lshl_add_u64 v[234:235], s[48:49], 0, v[152:153]
	ds_read_b128 v[184:187], v205 offset:32768
	ds_read_b128 v[188:191], v205 offset:33792
	ds_read_b128 v[192:195], v205 offset:34816
	ds_read_b128 v[206:209], v205 offset:35840
	ds_read_b128 v[210:213], v205 offset:36864
	ds_read_b128 v[214:217], v205 offset:37888
	ds_read_b128 v[218:221], v205 offset:38912
	ds_read_b128 v[222:225], v205 offset:39936
	global_load_lds_dwordx4 v[234:235], off
	v_lshl_add_u64 v[234:235], s[48:49], 0, v[156:157]
	s_mov_b32 m0, s25
	s_nop 0
	global_load_lds_dwordx4 v[234:235], off
	s_waitcnt vmcnt(8)
	s_waitcnt lgkmcnt(0)
	s_setprio 1
	s_waitcnt lgkmcnt(0)
	v_mfma_i32_16x16x64_i8 v[142:145], v[50:53], v[184:187], v[142:145]
	v_mfma_i32_16x16x64_i8 v[138:141], v[66:69], v[184:187], v[138:141]
	v_mfma_i32_16x16x64_i8 v[126:129], v[50:53], v[192:195], v[126:129]
	v_mfma_i32_16x16x64_i8 v[122:125], v[66:69], v[192:195], v[122:125]
	v_mfma_i32_16x16x64_i8 v[110:113], v[50:53], v[210:213], v[110:113]
	v_mfma_i32_16x16x64_i8 v[106:109], v[66:69], v[210:213], v[106:109]
	v_mfma_i32_16x16x64_i8 v[94:97], v[50:53], v[218:221], v[94:97]
	v_mfma_i32_16x16x64_i8 v[90:93], v[66:69], v[218:221], v[90:93]
	s_barrier
	v_mfma_i32_16x16x64_i8 v[142:145], v[54:57], v[188:191], v[142:145]
	v_mfma_i32_16x16x64_i8 v[138:141], v[70:73], v[188:191], v[138:141]
	v_mfma_i32_16x16x64_i8 v[126:129], v[54:57], v[206:209], v[126:129]
	v_mfma_i32_16x16x64_i8 v[122:125], v[70:73], v[206:209], v[122:125]
	v_mfma_i32_16x16x64_i8 v[110:113], v[54:57], v[214:217], v[110:113]
	v_mfma_i32_16x16x64_i8 v[106:109], v[70:73], v[214:217], v[106:109]
	v_mfma_i32_16x16x64_i8 v[94:97], v[54:57], v[222:225], v[94:97]
	v_mfma_i32_16x16x64_i8 v[90:93], v[70:73], v[222:225], v[90:93]
	s_setprio 0
	s_setprio 1
	v_mfma_i32_16x16x64_i8 v[134:137], v[168:171], v[184:187], v[134:137]
	v_mfma_i32_16x16x64_i8 v[130:133], v[176:179], v[184:187], v[130:133]
	v_mfma_i32_16x16x64_i8 v[118:121], v[168:171], v[192:195], v[118:121]
	v_mfma_i32_16x16x64_i8 v[114:117], v[176:179], v[192:195], v[114:117]
	v_mfma_i32_16x16x64_i8 v[102:105], v[168:171], v[210:213], v[102:105]
	v_mfma_i32_16x16x64_i8 v[98:101], v[176:179], v[210:213], v[98:101]
	v_mfma_i32_16x16x64_i8 v[86:89], v[168:171], v[218:221], v[86:89]
	v_mfma_i32_16x16x64_i8 v[82:85], v[176:179], v[218:221], v[82:85]
	v_mfma_i32_16x16x64_i8 v[134:137], v[172:175], v[188:191], v[134:137]
	v_mfma_i32_16x16x64_i8 v[130:133], v[180:183], v[188:191], v[130:133]
	v_mfma_i32_16x16x64_i8 v[118:121], v[172:175], v[206:209], v[118:121]
	v_mfma_i32_16x16x64_i8 v[114:117], v[180:183], v[206:209], v[114:117]
	v_mfma_i32_16x16x64_i8 v[102:105], v[172:175], v[214:217], v[102:105]
	v_mfma_i32_16x16x64_i8 v[98:101], v[180:183], v[214:217], v[98:101]
	v_mfma_i32_16x16x64_i8 v[86:89], v[172:175], v[222:225], v[86:89]
	v_mfma_i32_16x16x64_i8 v[82:85], v[180:183], v[222:225], v[82:85]
	s_setprio 0
	s_barrier
; #define PG8_STAGE(bufoff, gbase, voff) do { _Pragma("unroll") for (int _i = 0; _i < 2; ++_i) \
;         __builtin_amdgcn_global_load_lds((const unsigned*)((const char*)(gbase) + (voff)[_i]), (PG8_LAS unsigned*)(lds + (bufoff) + ldsw + _i * 8192), 16, 0, 0); } while (0)
; #define PG8_LDA(dst, b, h) do { _Pragma("unroll") for (int m = 0; m < 4; ++m) _Pragma("unroll") for (int k = 0; k < 2; ++k) dst[m][k] = *(const PG8_LAS bf16x8*)(lds + PG8_SA(b, h) + aoff + m * 2048 + k * 1024); } while (0)
; #define PG8_MMA(ai, bj, At, Bt) do { __builtin_amdgcn_s_setprio(1); _Pragma("unroll") for (int m = 0; m < 4; ++m) _Pragma("unroll") for (int n = 0; n < 2; ++n) _Pragma("unroll") for (int k = 0; k < 2; ++k) \
;         acc[ai][bj][m][n] = mma16<I8>(Bt[n][k], At[m][k], acc[ai][bj][m][n]); __builtin_amdgcn_s_setprio(0); } while (0)
; #define PG8_WAIT_V(n) asm volatile("s_waitcnt vmcnt(" #n ")" ::: "memory")
; #define PG8_WAIT_L(n) asm volatile("s_waitcnt lgkmcnt(" #n ")" ::: "memory")
; #define PG8_BAR __builtin_amdgcn_s_barrier()
; #define PG8_SCHED __builtin_amdgcn_sched_barrier(0)
; template <class Epi, class Sched, bool ALIGN_EPI = false, bool SP2 = false, bool I8 = false>
; __device__ __forceinline__ void gemm_phase(PG8_LAS unsigned char* lds, const Gemm g, const Sched& S, const Epi& E) {
;     ...
;         for (int t = 0; t < nt; t += 2) {
;     ...
;             PG8_LDA(At, 1, 1); PG8_STAGE(PG8_SB(1, 0), b3, voffB); PG8_STAGE(PG8_SB(1, 1), b3 + hstep, voffB); PG8_STAGE(PG8_SA(1, 0), a3, voffA);
;             PG8_WAIT_V(8); PG8_WAIT_L(0); PG8_BAR; PG8_MMA(1, 0, At, B0); PG8_MMA(1, 1, At, B1); PG8_BAR; PG8_SCHED;
	s_add_i32 s47, s47, s19
	v_lshl_add_u64 v[226:227], v[226:227], 0, s[14:15]
	s_mov_b32 m0, s47
	ds_read_b128 v[184:187], v205 offset:49152
	ds_read_b128 v[188:191], v205 offset:50176
	ds_read_b128 v[192:195], v205 offset:51200
	ds_read_b128 v[206:209], v205 offset:52224
	ds_read_b128 v[210:213], v205 offset:53248
	ds_read_b128 v[214:217], v205 offset:54272
	ds_read_b128 v[218:221], v205 offset:55296
	ds_read_b128 v[222:225], v205 offset:56320
	global_load_lds_dwordx4 v[226:227], off
	s_add_i32 m0, s47, 0x2000
	s_add_u32 s48, s62, 0x40080
	v_lshl_add_u64 v[226:227], v[228:229], 0, s[14:15]
	s_addc_u32 s49, s63, 0
	s_add_i32 s47, s50, s19
	global_load_lds_dwordx4 v[226:227], off
	v_lshl_add_u64 v[226:227], s[48:49], 0, v[154:155]
	s_mov_b32 m0, s47
	s_nop 0
	global_load_lds_dwordx4 v[226:227], off
	v_lshl_add_u64 v[226:227], s[48:49], 0, v[158:159]
	s_add_i32 m0, s47, 0x2000
	s_nop 0
	global_load_lds_dwordx4 v[226:227], off
	v_lshl_add_u64 v[226:227], v[230:231], 0, s[14:15]
	s_mov_b32 m0, s29
	s_nop 0
	global_load_lds_dwordx4 v[226:227], off
	v_lshl_add_u64 v[226:227], v[232:233], 0, s[14:15]
	s_mov_b32 m0, s31
	s_nop 0
	global_load_lds_dwordx4 v[226:227], off
	s_waitcnt vmcnt(8)
	s_waitcnt lgkmcnt(0)
	s_setprio 1
	s_waitcnt lgkmcnt(0)
	v_mfma_i32_16x16x64_i8 v[78:81], v[50:53], v[184:187], v[78:81]
	v_mfma_i32_16x16x64_i8 v[74:77], v[66:69], v[184:187], v[74:77]
	v_mfma_i32_16x16x64_i8 v[62:65], v[50:53], v[192:195], v[62:65]
	v_mfma_i32_16x16x64_i8 v[58:61], v[66:69], v[192:195], v[58:61]
	v_mfma_i32_16x16x64_i8 v[46:49], v[50:53], v[210:213], v[46:49]
	v_mfma_i32_16x16x64_i8 v[42:45], v[66:69], v[210:213], v[42:45]
	v_mfma_i32_16x16x64_i8 v[14:17], v[50:53], v[218:221], v[14:17]
	v_mfma_i32_16x16x64_i8 v[10:13], v[66:69], v[218:221], v[10:13]
	s_barrier
	v_mfma_i32_16x16x64_i8 v[78:81], v[54:57], v[188:191], v[78:81]
	v_mfma_i32_16x16x64_i8 v[74:77], v[70:73], v[188:191], v[74:77]
	v_mfma_i32_16x16x64_i8 v[62:65], v[54:57], v[206:209], v[62:65]
	v_mfma_i32_16x16x64_i8 v[58:61], v[70:73], v[206:209], v[58:61]
	v_mfma_i32_16x16x64_i8 v[46:49], v[54:57], v[214:217], v[46:49]
	v_mfma_i32_16x16x64_i8 v[42:45], v[70:73], v[214:217], v[42:45]
	v_mfma_i32_16x16x64_i8 v[14:17], v[54:57], v[222:225], v[14:17]
	v_mfma_i32_16x16x64_i8 v[10:13], v[70:73], v[222:225], v[10:13]
	s_setprio 0
	s_setprio 1
	v_mfma_i32_16x16x64_i8 v[22:25], v[168:171], v[184:187], v[22:25]
	v_mfma_i32_16x16x64_i8 v[70:73], v[172:175], v[188:191], v[22:25]
	v_mfma_i32_16x16x64_i8 v[22:25], v[176:179], v[184:187], v[30:33]
	v_mfma_i32_16x16x64_i8 v[66:69], v[180:183], v[188:191], v[22:25]
	v_mfma_i32_16x16x64_i8 v[22:25], v[168:171], v[192:195], v[34:37]
	v_mfma_i32_16x16x64_i8 v[54:57], v[172:175], v[206:209], v[22:25]
	v_mfma_i32_16x16x64_i8 v[22:25], v[176:179], v[192:195], v[38:41]
	v_mfma_i32_16x16x64_i8 v[50:53], v[180:183], v[206:209], v[22:25]
	v_mfma_i32_16x16x64_i8 v[22:25], v[168:171], v[210:213], v[26:29]
	v_mfma_i32_16x16x64_i8 v[18:21], v[176:179], v[210:213], v[18:21]
	v_mfma_i32_16x16x64_i8 v[6:9], v[168:171], v[218:221], v[6:9]
	v_mfma_i32_16x16x64_i8 v[2:5], v[176:179], v[218:221], v[2:5]
	v_mfma_i32_16x16x64_i8 v[26:29], v[172:175], v[214:217], v[22:25]
	v_mfma_i32_16x16x64_i8 v[18:21], v[180:183], v[214:217], v[18:21]
	v_mfma_i32_16x16x64_i8 v[6:9], v[172:175], v[222:225], v[6:9]
	v_mfma_i32_16x16x64_i8 v[2:5], v[180:183], v[222:225], v[2:5]
	s_setprio 0
	s_barrier
	s_add_i32 s46, s46, 2
	s_add_u32 s42, s42, 0x100
	s_addc_u32 s43, s43, 0
	s_add_u32 s44, s44, 0x100
	s_addc_u32 s45, s45, 0
	s_cmp_gt_u32 s46, 13
	s_cbranch_scc0 .LBB0_276
	s_and_b64 vcc, exec, s[16:17]
	s_cbranch_vccz .LBB0_279
	s_barrier

; #define PG8_STAGE(bufoff, gbase, voff) do { _Pragma("unroll") for (int _i = 0; _i < 2; ++_i) \
;         __builtin_amdgcn_global_load_lds((const unsigned*)((const char*)(gbase) + (voff)[_i]), (PG8_LAS unsigned*)(lds + (bufoff) + ldsw + _i * 8192), 16, 0, 0); } while (0)
; #define PG8_LDA(dst, b, h) do { _Pragma("unroll") for (int m = 0; m < 4; ++m) _Pragma("unroll") for (int k = 0; k < 2; ++k) dst[m][k] = *(const PG8_LAS bf16x8*)(lds + PG8_SA(b, h) + aoff + m * 2048 + k * 1024); } while (0)
; #define PG8_LDB(dst, b, h) do { _Pragma("unroll") for (int n = 0; n < 2; ++n) _Pragma("unroll") for (int k = 0; k < 2; ++k) dst[n][k] = *(const PG8_LAS bf16x8*)(lds + PG8_SB(b, h) + boff + n * 2048 + k * 1024); } while (0)
; #define PG8_MMA(ai, bj, At, Bt) do { __builtin_amdgcn_s_setprio(1); _Pragma("unroll") for (int m = 0; m < 4; ++m) _Pragma("unroll") for (int n = 0; n < 2; ++n) _Pragma("unroll") for (int k = 0; k < 2; ++k) \
;         acc[ai][bj][m][n] = mma16<I8>(Bt[n][k], At[m][k], acc[ai][bj][m][n]); __builtin_amdgcn_s_setprio(0); } while (0)
; #define PG8_WAIT_V(n) asm volatile("s_waitcnt vmcnt(" #n ")" ::: "memory")
; #define PG8_WAIT_L(n) asm volatile("s_waitcnt lgkmcnt(" #n ")" ::: "memory")
; #define PG8_BAR __builtin_amdgcn_s_barrier()
; #define PG8_SCHED __builtin_amdgcn_sched_barrier(0)
; template <class Epi, class Sched, bool ALIGN_EPI = false, bool SP2 = false, bool I8 = false>
; __device__ __forceinline__ void gemm_phase(PG8_LAS unsigned char* lds, const Gemm g, const Sched& S, const Epi& E) {
;     ...
;             PG8_LDB(B0, 0, 0); PG8_LDB(B1, 0, 1); PG8_SCHED; PG8_LDA(At, 0, 0); PG8_STAGE(PG8_SA(1, 1), a1 + hstep, voffA);
;             PG8_WAIT_V(8); PG8_WAIT_L(0); PG8_BAR; PG8_MMA(0, 0, At, B0); PG8_MMA(0, 1, At, B1); PG8_BAR; PG8_SCHED;
;             PG8_LDA(At, 0, 1); PG8_STAGE(PG8_SB(0, 0), b2, voffB); PG8_STAGE(PG8_SB(0, 1), b2 + hstep, voffB); PG8_STAGE(PG8_SA(0, 0), a2, voffA);
;             PG8_WAIT_V(8); PG8_WAIT_L(0); PG8_BAR; PG8_MMA(1, 0, At, B0); PG8_MMA(1, 1, At, B1); PG8_BAR; PG8_SCHED;
.LBB0_334:
	ds_read_b128 v[22:25], v1
	ds_read_b128 v[26:29], v1 offset:1024
	ds_read_b128 v[34:37], v1 offset:2048
	ds_read_b128 v[38:41], v1 offset:3072
	ds_read_b128 v[168:171], v147
	ds_read_b128 v[172:175], v147 offset:1024
	ds_read_b128 v[176:179], v147 offset:2048
	ds_read_b128 v[180:183], v147 offset:3072
	s_add_u32 s42, s40, 0xfffc0080
	s_addc_u32 s43, s41, -1
	s_cmp_eq_u32 s46, 12
	s_cselect_b32 s63, s5, s43
	s_cselect_b32 s62, s33, s42
	s_cselect_b32 s43, s31, s45
	s_cselect_b32 s42, s35, s44
	v_lshl_add_u64 v[198:199], s[40:41], 0, v[160:161]
	s_add_i32 m0, s3, 0xc000
	ds_read_b128 v[184:187], v149
	ds_read_b128 v[188:191], v149 offset:1024
	ds_read_b128 v[192:195], v149 offset:2048
	ds_read_b128 v[202:205], v149 offset:3072
	ds_read_b128 v[206:209], v149 offset:4096
	ds_read_b128 v[210:213], v149 offset:5120
	ds_read_b128 v[214:217], v149 offset:6144
	ds_read_b128 v[218:221], v149 offset:7168
	global_load_lds_dwordx4 v[198:199], off
	v_lshl_add_u64 v[198:199], s[40:41], 0, v[162:163]
	s_add_i32 m0, s3, 0xe000
	s_nop 0
	global_load_lds_dwordx4 v[198:199], off
	s_waitcnt vmcnt(8)
	s_waitcnt lgkmcnt(0)
	s_setprio 1
	s_waitcnt lgkmcnt(0)
	v_mfma_i32_16x16x64_i8 v[142:145], v[22:25], v[184:187], v[142:145]
	v_mfma_i32_16x16x64_i8 v[138:141], v[34:37], v[184:187], v[138:141]
	v_mfma_i32_16x16x64_i8 v[126:129], v[22:25], v[192:195], v[126:129]
	v_mfma_i32_16x16x64_i8 v[122:125], v[34:37], v[192:195], v[122:125]
	v_mfma_i32_16x16x64_i8 v[110:113], v[22:25], v[206:209], v[110:113]
	v_mfma_i32_16x16x64_i8 v[106:109], v[34:37], v[206:209], v[106:109]
	v_mfma_i32_16x16x64_i8 v[94:97], v[22:25], v[214:217], v[94:97]
	v_mfma_i32_16x16x64_i8 v[90:93], v[34:37], v[214:217], v[90:93]
	s_barrier
	v_mfma_i32_16x16x64_i8 v[142:145], v[26:29], v[188:191], v[142:145]
	v_mfma_i32_16x16x64_i8 v[138:141], v[38:41], v[188:191], v[138:141]
	v_mfma_i32_16x16x64_i8 v[126:129], v[26:29], v[202:205], v[126:129]
	v_mfma_i32_16x16x64_i8 v[122:125], v[38:41], v[202:205], v[122:125]
	v_mfma_i32_16x16x64_i8 v[110:113], v[26:29], v[210:213], v[110:113]
	v_mfma_i32_16x16x64_i8 v[106:109], v[38:41], v[210:213], v[106:109]
	v_mfma_i32_16x16x64_i8 v[94:97], v[26:29], v[218:221], v[94:97]
	v_mfma_i32_16x16x64_i8 v[90:93], v[38:41], v[218:221], v[90:93]
	s_setprio 0
	s_setprio 1
	v_mfma_i32_16x16x64_i8 v[134:137], v[168:171], v[184:187], v[134:137]
	v_mfma_i32_16x16x64_i8 v[130:133], v[176:179], v[184:187], v[130:133]
	v_mfma_i32_16x16x64_i8 v[118:121], v[168:171], v[192:195], v[118:121]
	v_mfma_i32_16x16x64_i8 v[114:117], v[176:179], v[192:195], v[114:117]
	v_mfma_i32_16x16x64_i8 v[102:105], v[168:171], v[206:209], v[102:105]
	v_mfma_i32_16x16x64_i8 v[98:101], v[176:179], v[206:209], v[98:101]
	v_mfma_i32_16x16x64_i8 v[86:89], v[168:171], v[214:217], v[86:89]
	v_mfma_i32_16x16x64_i8 v[82:85], v[176:179], v[214:217], v[82:85]
	v_mfma_i32_16x16x64_i8 v[134:137], v[172:175], v[188:191], v[134:137]
	v_mfma_i32_16x16x64_i8 v[130:133], v[180:183], v[188:191], v[130:133]
	v_mfma_i32_16x16x64_i8 v[118:121], v[172:175], v[202:205], v[118:121]
	v_mfma_i32_16x16x64_i8 v[114:117], v[180:183], v[202:205], v[114:117]
	v_mfma_i32_16x16x64_i8 v[102:105], v[172:175], v[210:213], v[102:105]
	v_mfma_i32_16x16x64_i8 v[98:101], v[180:183], v[210:213], v[98:101]
	v_mfma_i32_16x16x64_i8 v[86:89], v[172:175], v[218:221], v[86:89]
	v_mfma_i32_16x16x64_i8 v[82:85], v[180:183], v[218:221], v[82:85]
	s_setprio 0
	s_barrier
	s_add_i32 s47, s84, s21
	v_lshl_add_u64 v[198:199], s[42:43], 0, v[154:155]
	s_mov_b32 m0, s47
	ds_read_b128 v[184:187], v149 offset:16384
	ds_read_b128 v[188:191], v149 offset:17408
	ds_read_b128 v[192:195], v149 offset:18432
	ds_read_b128 v[202:205], v149 offset:19456
	ds_read_b128 v[206:209], v149 offset:20480
	ds_read_b128 v[210:213], v149 offset:21504
	ds_read_b128 v[214:217], v149 offset:22528
	ds_read_b128 v[218:221], v149 offset:23552
	global_load_lds_dwordx4 v[198:199], off
	s_add_i32 m0, s47, 0x2000
	s_add_u32 s48, s42, 0x40000
	v_lshl_add_u64 v[222:223], s[42:43], 0, v[158:159]
	s_addc_u32 s49, s43, 0
	s_add_i32 s47, s85, s21
	global_load_lds_dwordx4 v[222:223], off
	v_lshl_add_u64 v[224:225], s[48:49], 0, v[154:155]
	s_mov_b32 m0, s47
	v_lshl_add_u64 v[226:227], s[62:63], 0, v[156:157]
	global_load_lds_dwordx4 v[224:225], off
	v_lshl_add_u64 v[224:225], s[48:49], 0, v[158:159]
	s_add_i32 m0, s47, 0x2000
	s_nop 0
	global_load_lds_dwordx4 v[224:225], off
	v_lshl_add_u64 v[224:225], s[62:63], 0, v[152:153]
	s_mov_b32 m0, s3
	s_nop 0
	global_load_lds_dwordx4 v[224:225], off
	s_mov_b32 m0, s23
	s_nop 0
	global_load_lds_dwordx4 v[226:227], off
	s_waitcnt vmcnt(8)
	s_waitcnt lgkmcnt(0)
	s_setprio 1
	s_waitcnt lgkmcnt(0)
	v_mfma_i32_16x16x64_i8 v[78:81], v[22:25], v[184:187], v[78:81]
	v_mfma_i32_16x16x64_i8 v[74:77], v[34:37], v[184:187], v[74:77]
	v_mfma_i32_16x16x64_i8 v[62:65], v[22:25], v[192:195], v[62:65]
	v_mfma_i32_16x16x64_i8 v[58:61], v[34:37], v[192:195], v[58:61]
	v_mfma_i32_16x16x64_i8 v[46:49], v[22:25], v[206:209], v[46:49]
	v_mfma_i32_16x16x64_i8 v[42:45], v[34:37], v[206:209], v[42:45]
	v_mfma_i32_16x16x64_i8 v[14:17], v[22:25], v[214:217], v[14:17]
	v_mfma_i32_16x16x64_i8 v[10:13], v[34:37], v[214:217], v[10:13]
	s_barrier
; #define PG8_STAGE(bufoff, gbase, voff) do { _Pragma("unroll") for (int _i = 0; _i < 2; ++_i) \
;         __builtin_amdgcn_global_load_lds((const unsigned*)((const char*)(gbase) + (voff)[_i]), (PG8_LAS unsigned*)(lds + (bufoff) + ldsw + _i * 8192), 16, 0, 0); } while (0)
; #define PG8_LDA(dst, b, h) do { _Pragma("unroll") for (int m = 0; m < 4; ++m) _Pragma("unroll") for (int k = 0; k < 2; ++k) dst[m][k] = *(const PG8_LAS bf16x8*)(lds + PG8_SA(b, h) + aoff + m * 2048 + k * 1024); } while (0)
; #define PG8_LDB(dst, b, h) do { _Pragma("unroll") for (int n = 0; n < 2; ++n) _Pragma("unroll") for (int k = 0; k < 2; ++k) dst[n][k] = *(const PG8_LAS bf16x8*)(lds + PG8_SB(b, h) + boff + n * 2048 + k * 1024); } while (0)
; #define PG8_MMA(ai, bj, At, Bt) do { __builtin_amdgcn_s_setprio(1); _Pragma("unroll") for (int m = 0; m < 4; ++m) _Pragma("unroll") for (int n = 0; n < 2; ++n) _Pragma("unroll") for (int k = 0; k < 2; ++k) \
;         acc[ai][bj][m][n] = mma16<I8>(Bt[n][k], At[m][k], acc[ai][bj][m][n]); __builtin_amdgcn_s_setprio(0); } while (0)
; #define PG8_WAIT_V(n) asm volatile("s_waitcnt vmcnt(" #n ")" ::: "memory")
; #define PG8_WAIT_L(n) asm volatile("s_waitcnt lgkmcnt(" #n ")" ::: "memory")
; #define PG8_BAR __builtin_amdgcn_s_barrier()
; #define PG8_SCHED __builtin_amdgcn_sched_barrier(0)
; template <class Epi, class Sched, bool ALIGN_EPI = false, bool SP2 = false, bool I8 = false>
; __device__ __forceinline__ void gemm_phase(PG8_LAS unsigned char* lds, const Gemm g, const Sched& S, const Epi& E) {
;     ...
;             PG8_WAIT_V(8); PG8_WAIT_L(0); PG8_BAR; PG8_MMA(1, 0, At, B0); PG8_MMA(1, 1, At, B1); PG8_BAR; PG8_SCHED;
;             PG8_LDB(B0, 1, 0); PG8_LDB(B1, 1, 1); PG8_SCHED; PG8_LDA(At, 1, 0); PG8_STAGE(PG8_SA(0, 1), a2 + hstep, voffA);
;             PG8_WAIT_V(8); PG8_WAIT_L(0); PG8_BAR; PG8_MMA(0, 0, At, B0); PG8_MMA(0, 1, At, B1); PG8_BAR; PG8_SCHED;
	v_mfma_i32_16x16x64_i8 v[78:81], v[26:29], v[188:191], v[78:81]
	v_mfma_i32_16x16x64_i8 v[74:77], v[38:41], v[188:191], v[74:77]
	v_mfma_i32_16x16x64_i8 v[62:65], v[26:29], v[202:205], v[62:65]
	v_mfma_i32_16x16x64_i8 v[58:61], v[38:41], v[202:205], v[58:61]
	v_mfma_i32_16x16x64_i8 v[46:49], v[26:29], v[210:213], v[46:49]
	v_mfma_i32_16x16x64_i8 v[42:45], v[38:41], v[210:213], v[42:45]
	v_mfma_i32_16x16x64_i8 v[14:17], v[26:29], v[218:221], v[14:17]
	v_mfma_i32_16x16x64_i8 v[10:13], v[38:41], v[218:221], v[10:13]
	s_setprio 0
	s_setprio 1
	v_mfma_i32_16x16x64_i8 v[30:33], v[168:171], v[206:209], v[30:33]
	v_mfma_i32_16x16x64_i8 v[18:21], v[176:179], v[206:209], v[18:21]
	v_mfma_i32_16x16x64_i8 v[6:9], v[168:171], v[214:217], v[6:9]
	v_mfma_i32_16x16x64_i8 v[2:5], v[176:179], v[214:217], v[2:5]
	v_mfma_i32_16x16x64_i8 v[22:25], v[168:171], v[184:187], v[70:73]
	v_mfma_i32_16x16x64_i8 v[26:29], v[176:179], v[184:187], v[66:69]
	v_mfma_i32_16x16x64_i8 v[34:37], v[168:171], v[192:195], v[54:57]
	v_mfma_i32_16x16x64_i8 v[38:41], v[176:179], v[192:195], v[50:53]
	v_mfma_i32_16x16x64_i8 v[30:33], v[172:175], v[210:213], v[30:33]
	v_mfma_i32_16x16x64_i8 v[18:21], v[180:183], v[210:213], v[18:21]
	v_mfma_i32_16x16x64_i8 v[6:9], v[172:175], v[218:221], v[6:9]
	v_mfma_i32_16x16x64_i8 v[2:5], v[180:183], v[218:221], v[2:5]
	v_mfma_i32_16x16x64_i8 v[22:25], v[172:175], v[188:191], v[22:25]
	v_mfma_i32_16x16x64_i8 v[26:29], v[180:183], v[188:191], v[26:29]
	v_mfma_i32_16x16x64_i8 v[34:37], v[172:175], v[202:205], v[34:37]
	v_mfma_i32_16x16x64_i8 v[38:41], v[180:183], v[202:205], v[38:41]
	s_setprio 0
	s_barrier
	s_add_i32 s47, 0, 0x18000
	s_add_i32 s50, 0, 0x1c000
	v_add_u32_e32 v70, s47, v197
	v_add_u32_e32 v151, s50, v197
	ds_read_b128 v[50:53], v70
	ds_read_b128 v[54:57], v70 offset:1024
	ds_read_b128 v[66:69], v70 offset:2048
	ds_read_b128 v[70:73], v70 offset:3072
	ds_read_b128 v[168:171], v151
	ds_read_b128 v[172:175], v151 offset:1024
	ds_read_b128 v[176:179], v151 offset:2048
	ds_read_b128 v[180:183], v151 offset:3072
	s_add_u32 s48, s62, 0x40000
	s_addc_u32 s49, s63, 0
	s_mov_b32 m0, s25
	v_lshl_add_u64 v[228:229], s[48:49], 0, v[152:153]
	ds_read_b128 v[184:187], v149 offset:32768
	ds_read_b128 v[188:191], v149 offset:33792
	ds_read_b128 v[192:195], v149 offset:34816
	ds_read_b128 v[202:205], v149 offset:35840
	ds_read_b128 v[206:209], v149 offset:36864
	ds_read_b128 v[210:213], v149 offset:37888
	ds_read_b128 v[214:217], v149 offset:38912
	ds_read_b128 v[218:221], v149 offset:39936
	global_load_lds_dwordx4 v[228:229], off
	v_lshl_add_u64 v[228:229], s[48:49], 0, v[156:157]
	s_mov_b32 m0, s27
	s_nop 0
	global_load_lds_dwordx4 v[228:229], off
	s_waitcnt vmcnt(8)
	s_waitcnt lgkmcnt(0)
	s_setprio 1
	s_waitcnt lgkmcnt(0)
	v_mfma_i32_16x16x64_i8 v[142:145], v[50:53], v[184:187], v[142:145]
	v_mfma_i32_16x16x64_i8 v[138:141], v[66:69], v[184:187], v[138:141]
	v_mfma_i32_16x16x64_i8 v[126:129], v[50:53], v[192:195], v[126:129]
	v_mfma_i32_16x16x64_i8 v[122:125], v[66:69], v[192:195], v[122:125]
	v_mfma_i32_16x16x64_i8 v[110:113], v[50:53], v[206:209], v[110:113]
	v_mfma_i32_16x16x64_i8 v[106:109], v[66:69], v[206:209], v[106:109]
	v_mfma_i32_16x16x64_i8 v[94:97], v[50:53], v[214:217], v[94:97]
	v_mfma_i32_16x16x64_i8 v[90:93], v[66:69], v[214:217], v[90:93]
	s_barrier
	v_mfma_i32_16x16x64_i8 v[142:145], v[54:57], v[188:191], v[142:145]
	v_mfma_i32_16x16x64_i8 v[138:141], v[70:73], v[188:191], v[138:141]
	v_mfma_i32_16x16x64_i8 v[126:129], v[54:57], v[202:205], v[126:129]
	v_mfma_i32_16x16x64_i8 v[122:125], v[70:73], v[202:205], v[122:125]
	v_mfma_i32_16x16x64_i8 v[110:113], v[54:57], v[210:213], v[110:113]
	v_mfma_i32_16x16x64_i8 v[106:109], v[70:73], v[210:213], v[106:109]
	v_mfma_i32_16x16x64_i8 v[94:97], v[54:57], v[218:221], v[94:97]
	v_mfma_i32_16x16x64_i8 v[90:93], v[70:73], v[218:221], v[90:93]
	s_setprio 0
	s_setprio 1
	v_mfma_i32_16x16x64_i8 v[134:137], v[168:171], v[184:187], v[134:137]
	v_mfma_i32_16x16x64_i8 v[130:133], v[176:179], v[184:187], v[130:133]
	v_mfma_i32_16x16x64_i8 v[118:121], v[168:171], v[192:195], v[118:121]
	v_mfma_i32_16x16x64_i8 v[114:117], v[176:179], v[192:195], v[114:117]
	v_mfma_i32_16x16x64_i8 v[102:105], v[168:171], v[206:209], v[102:105]
	v_mfma_i32_16x16x64_i8 v[98:101], v[176:179], v[206:209], v[98:101]
	v_mfma_i32_16x16x64_i8 v[86:89], v[168:171], v[214:217], v[86:89]
	v_mfma_i32_16x16x64_i8 v[82:85], v[176:179], v[214:217], v[82:85]
	v_mfma_i32_16x16x64_i8 v[134:137], v[172:175], v[188:191], v[134:137]
	v_mfma_i32_16x16x64_i8 v[130:133], v[180:183], v[188:191], v[130:133]
	v_mfma_i32_16x16x64_i8 v[118:121], v[172:175], v[202:205], v[118:121]
	v_mfma_i32_16x16x64_i8 v[114:117], v[180:183], v[202:205], v[114:117]
	v_mfma_i32_16x16x64_i8 v[102:105], v[172:175], v[210:213], v[102:105]
	v_mfma_i32_16x16x64_i8 v[98:101], v[180:183], v[210:213], v[98:101]
	v_mfma_i32_16x16x64_i8 v[86:89], v[172:175], v[218:221], v[86:89]
	v_mfma_i32_16x16x64_i8 v[82:85], v[180:183], v[218:221], v[82:85]
	s_setprio 0
	s_barrier
; #define PG8_STAGE(bufoff, gbase, voff) do { _Pragma("unroll") for (int _i = 0; _i < 2; ++_i) \
;         __builtin_amdgcn_global_load_lds((const unsigned*)((const char*)(gbase) + (voff)[_i]), (PG8_LAS unsigned*)(lds + (bufoff) + ldsw + _i * 8192), 16, 0, 0); } while (0)
; #define PG8_LDA(dst, b, h) do { _Pragma("unroll") for (int m = 0; m < 4; ++m) _Pragma("unroll") for (int k = 0; k < 2; ++k) dst[m][k] = *(const PG8_LAS bf16x8*)(lds + PG8_SA(b, h) + aoff + m * 2048 + k * 1024); } while (0)
; #define PG8_MMA(ai, bj, At, Bt) do { __builtin_amdgcn_s_setprio(1); _Pragma("unroll") for (int m = 0; m < 4; ++m) _Pragma("unroll") for (int n = 0; n < 2; ++n) _Pragma("unroll") for (int k = 0; k < 2; ++k) \
;         acc[ai][bj][m][n] = mma16<I8>(Bt[n][k], At[m][k], acc[ai][bj][m][n]); __builtin_amdgcn_s_setprio(0); } while (0)
; #define PG8_WAIT_V(n) asm volatile("s_waitcnt vmcnt(" #n ")" ::: "memory")
; #define PG8_WAIT_L(n) asm volatile("s_waitcnt lgkmcnt(" #n ")" ::: "memory")
; #define PG8_BAR __builtin_amdgcn_s_barrier()
; #define PG8_SCHED __builtin_amdgcn_sched_barrier(0)
; template <class Epi, class Sched, bool ALIGN_EPI = false, bool SP2 = false, bool I8 = false>
; __device__ __forceinline__ void gemm_phase(PG8_LAS unsigned char* lds, const Gemm g, const Sched& S, const Epi& E) {
;     ...
;         for (int t = 0; t < nt; t += 2) {
;     ...
;             PG8_LDA(At, 1, 1); PG8_STAGE(PG8_SB(1, 0), b3, voffB); PG8_STAGE(PG8_SB(1, 1), b3 + hstep, voffB); PG8_STAGE(PG8_SA(1, 0), a3, voffA);
;             PG8_WAIT_V(8); PG8_WAIT_L(0); PG8_BAR; PG8_MMA(1, 0, At, B0); PG8_MMA(1, 1, At, B1); PG8_BAR; PG8_SCHED;
	s_add_i32 s47, s47, s21
	v_lshl_add_u64 v[198:199], v[198:199], 0, s[12:13]
	s_mov_b32 m0, s47
	ds_read_b128 v[184:187], v149 offset:49152
	ds_read_b128 v[188:191], v149 offset:50176
	ds_read_b128 v[192:195], v149 offset:51200
	ds_read_b128 v[202:205], v149 offset:52224
	ds_read_b128 v[206:209], v149 offset:53248
	ds_read_b128 v[210:213], v149 offset:54272
	ds_read_b128 v[214:217], v149 offset:55296
	ds_read_b128 v[218:221], v149 offset:56320
	global_load_lds_dwordx4 v[198:199], off
	s_add_i32 m0, s47, 0x2000
	s_add_u32 s42, s42, 0x40080
	v_lshl_add_u64 v[198:199], v[222:223], 0, s[12:13]
	s_addc_u32 s43, s43, 0
	s_add_i32 s47, s50, s21
	global_load_lds_dwordx4 v[198:199], off
	v_lshl_add_u64 v[198:199], s[42:43], 0, v[154:155]
	s_mov_b32 m0, s47
	s_nop 0
	global_load_lds_dwordx4 v[198:199], off
	v_lshl_add_u64 v[198:199], s[42:43], 0, v[158:159]
	s_add_i32 m0, s47, 0x2000
	s_nop 0
	global_load_lds_dwordx4 v[198:199], off
	v_lshl_add_u64 v[198:199], v[224:225], 0, s[12:13]
	s_mov_b32 m0, s68
	s_nop 0
	global_load_lds_dwordx4 v[198:199], off
	v_lshl_add_u64 v[198:199], v[226:227], 0, s[12:13]
	s_mov_b32 m0, s69
	s_nop 0
	global_load_lds_dwordx4 v[198:199], off
	s_waitcnt vmcnt(8)
	s_waitcnt lgkmcnt(0)
	s_setprio 1
	s_waitcnt lgkmcnt(0)
	v_mfma_i32_16x16x64_i8 v[78:81], v[50:53], v[184:187], v[78:81]
	v_mfma_i32_16x16x64_i8 v[74:77], v[66:69], v[184:187], v[74:77]
	v_mfma_i32_16x16x64_i8 v[62:65], v[50:53], v[192:195], v[62:65]
	v_mfma_i32_16x16x64_i8 v[58:61], v[66:69], v[192:195], v[58:61]
	v_mfma_i32_16x16x64_i8 v[46:49], v[50:53], v[206:209], v[46:49]
	v_mfma_i32_16x16x64_i8 v[42:45], v[66:69], v[206:209], v[42:45]
	v_mfma_i32_16x16x64_i8 v[14:17], v[50:53], v[214:217], v[14:17]
	v_mfma_i32_16x16x64_i8 v[10:13], v[66:69], v[214:217], v[10:13]
	s_barrier
	v_mfma_i32_16x16x64_i8 v[78:81], v[54:57], v[188:191], v[78:81]
	v_mfma_i32_16x16x64_i8 v[74:77], v[70:73], v[188:191], v[74:77]
	v_mfma_i32_16x16x64_i8 v[62:65], v[54:57], v[202:205], v[62:65]
	v_mfma_i32_16x16x64_i8 v[58:61], v[70:73], v[202:205], v[58:61]
	v_mfma_i32_16x16x64_i8 v[46:49], v[54:57], v[210:213], v[46:49]
	v_mfma_i32_16x16x64_i8 v[42:45], v[70:73], v[210:213], v[42:45]
	v_mfma_i32_16x16x64_i8 v[14:17], v[54:57], v[218:221], v[14:17]
	v_mfma_i32_16x16x64_i8 v[10:13], v[70:73], v[218:221], v[10:13]
	s_setprio 0
	s_setprio 1
	v_mfma_i32_16x16x64_i8 v[22:25], v[168:171], v[184:187], v[22:25]
	v_mfma_i32_16x16x64_i8 v[70:73], v[172:175], v[188:191], v[22:25]
	v_mfma_i32_16x16x64_i8 v[22:25], v[176:179], v[184:187], v[26:29]
	v_mfma_i32_16x16x64_i8 v[66:69], v[180:183], v[188:191], v[22:25]
	v_mfma_i32_16x16x64_i8 v[22:25], v[168:171], v[192:195], v[34:37]
	v_mfma_i32_16x16x64_i8 v[54:57], v[172:175], v[202:205], v[22:25]
	v_mfma_i32_16x16x64_i8 v[22:25], v[176:179], v[192:195], v[38:41]
	v_mfma_i32_16x16x64_i8 v[50:53], v[180:183], v[202:205], v[22:25]
	v_mfma_i32_16x16x64_i8 v[22:25], v[168:171], v[206:209], v[30:33]
	v_mfma_i32_16x16x64_i8 v[18:21], v[176:179], v[206:209], v[18:21]
	v_mfma_i32_16x16x64_i8 v[6:9], v[168:171], v[214:217], v[6:9]
	v_mfma_i32_16x16x64_i8 v[2:5], v[176:179], v[214:217], v[2:5]
	v_mfma_i32_16x16x64_i8 v[30:33], v[172:175], v[210:213], v[22:25]
	v_mfma_i32_16x16x64_i8 v[18:21], v[180:183], v[210:213], v[18:21]
	v_mfma_i32_16x16x64_i8 v[6:9], v[172:175], v[218:221], v[6:9]
	v_mfma_i32_16x16x64_i8 v[2:5], v[180:183], v[218:221], v[2:5]
	s_setprio 0
	s_barrier
	s_add_i32 s46, s46, 2
	s_add_u32 s40, s40, 0x100
	s_addc_u32 s41, s41, 0
	s_add_u32 s44, s44, 0x100
	s_addc_u32 s45, s45, 0
	s_cmp_gt_u32 s46, 13
	s_cbranch_scc0 .LBB0_334
	s_and_b64 vcc, exec, s[14:15]
	s_cbranch_vccz .LBB0_337
	s_barrier

; #define PG8_STAGE(bufoff, gbase, voff) do { _Pragma("unroll") for (int _i = 0; _i < 2; ++_i) \
;         __builtin_amdgcn_global_load_lds((const unsigned*)((const char*)(gbase) + (voff)[_i]), (PG8_LAS unsigned*)(lds + (bufoff) + ldsw + _i * 8192), 16, 0, 0); } while (0)
; #define PG8_LDA(dst, b, h) do { _Pragma("unroll") for (int m = 0; m < 4; ++m) _Pragma("unroll") for (int k = 0; k < 2; ++k) dst[m][k] = *(const PG8_LAS bf16x8*)(lds + PG8_SA(b, h) + aoff + m * 2048 + k * 1024); } while (0)
; #define PG8_LDB(dst, b, h) do { _Pragma("unroll") for (int n = 0; n < 2; ++n) _Pragma("unroll") for (int k = 0; k < 2; ++k) dst[n][k] = *(const PG8_LAS bf16x8*)(lds + PG8_SB(b, h) + boff + n * 2048 + k * 1024); } while (0)
; #define PG8_MMA(ai, bj, At, Bt) do { __builtin_amdgcn_s_setprio(1); _Pragma("unroll") for (int m = 0; m < 4; ++m) _Pragma("unroll") for (int n = 0; n < 2; ++n) _Pragma("unroll") for (int k = 0; k < 2; ++k) \
;         acc[ai][bj][m][n] = mma16<I8>(Bt[n][k], At[m][k], acc[ai][bj][m][n]); __builtin_amdgcn_s_setprio(0); } while (0)
; #define PG8_WAIT_V(n) asm volatile("s_waitcnt vmcnt(" #n ")" ::: "memory")
; #define PG8_WAIT_L(n) asm volatile("s_waitcnt lgkmcnt(" #n ")" ::: "memory")
; #define PG8_BAR __builtin_amdgcn_s_barrier()
; #define PG8_SCHED __builtin_amdgcn_sched_barrier(0)
; template <class Epi, class Sched, bool ALIGN_EPI = false, bool SP2 = false, bool I8 = false>
; __device__ __forceinline__ void gemm_phase(PG8_LAS unsigned char* lds, const Gemm g, const Sched& S, const Epi& E) {
;     ...
;             PG8_LDB(B0, 0, 0); PG8_LDB(B1, 0, 1); PG8_SCHED; PG8_LDA(At, 0, 0); PG8_STAGE(PG8_SA(1, 1), a1 + hstep, voffA);
;             PG8_WAIT_V(8); PG8_WAIT_L(0); PG8_BAR; PG8_MMA(0, 0, At, B0); PG8_MMA(0, 1, At, B1); PG8_BAR; PG8_SCHED;
;             PG8_LDA(At, 0, 1); PG8_STAGE(PG8_SB(0, 0), b2, voffB); PG8_STAGE(PG8_SB(0, 1), b2 + hstep, voffB); PG8_STAGE(PG8_SA(0, 0), a2, voffA);
;             PG8_WAIT_V(8); PG8_WAIT_L(0); PG8_BAR; PG8_MMA(1, 0, At, B0); PG8_MMA(1, 1, At, B1); PG8_BAR; PG8_SCHED;
.LBB0_974:
	ds_read_b128 v[130:133], v163
	ds_read_b128 v[134:137], v163 offset:1024
	ds_read_b128 v[164:167], v163 offset:2048
	ds_read_b128 v[168:171], v163 offset:3072
	ds_read_b128 v[172:175], v181
	ds_read_b128 v[176:179], v181 offset:1024
	ds_read_b128 v[184:187], v181 offset:2048
	ds_read_b128 v[188:191], v181 offset:3072
	s_add_u32 s42, s40, 0xfffc0080
	s_addc_u32 s43, s41, -1
	s_cmp_eq_u32 s63, 12
	s_cselect_b32 s45, s31, s43
	s_cselect_b32 s44, s57, s42
	s_cselect_b32 s43, s29, s62
	s_cselect_b32 s42, s58, s59
	v_lshl_add_u64 v[160:161], s[40:41], 0, v[152:153]
	s_add_i32 m0, s39, 0xc000
	ds_read_b128 v[192:195], v183
	ds_read_b128 v[202:205], v183 offset:1024
	ds_read_b128 v[206:209], v183 offset:2048
	ds_read_b128 v[210:213], v183 offset:3072
	ds_read_b128 v[214:217], v183 offset:4096
	ds_read_b128 v[218:221], v183 offset:5120
	ds_read_b128 v[222:225], v183 offset:6144
	ds_read_b128 v[226:229], v183 offset:7168
	global_load_lds_dwordx4 v[160:161], off
	v_lshl_add_u64 v[160:161], s[40:41], 0, v[154:155]
	s_add_i32 m0, s39, 0xe000
	s_nop 0
	global_load_lds_dwordx4 v[160:161], off
	s_waitcnt vmcnt(8)
	s_waitcnt lgkmcnt(0)
	s_setprio 1
	s_waitcnt lgkmcnt(0)
	v_mfma_i32_16x16x64_i8 v[126:129], v[130:133], v[192:195], v[126:129]
	v_mfma_i32_16x16x64_i8 v[122:125], v[164:167], v[192:195], v[122:125]
	v_mfma_i32_16x16x64_i8 v[110:113], v[130:133], v[206:209], v[110:113]
	v_mfma_i32_16x16x64_i8 v[106:109], v[164:167], v[206:209], v[106:109]
	v_mfma_i32_16x16x64_i8 v[94:97], v[130:133], v[214:217], v[94:97]
	v_mfma_i32_16x16x64_i8 v[90:93], v[164:167], v[214:217], v[90:93]
	v_mfma_i32_16x16x64_i8 v[78:81], v[130:133], v[222:225], v[78:81]
	v_mfma_i32_16x16x64_i8 v[74:77], v[164:167], v[222:225], v[74:77]
	s_barrier
	v_mfma_i32_16x16x64_i8 v[126:129], v[134:137], v[202:205], v[126:129]
	v_mfma_i32_16x16x64_i8 v[122:125], v[168:171], v[202:205], v[122:125]
	v_mfma_i32_16x16x64_i8 v[110:113], v[134:137], v[210:213], v[110:113]
	v_mfma_i32_16x16x64_i8 v[106:109], v[168:171], v[210:213], v[106:109]
	v_mfma_i32_16x16x64_i8 v[94:97], v[134:137], v[218:221], v[94:97]
	v_mfma_i32_16x16x64_i8 v[90:93], v[168:171], v[218:221], v[90:93]
	v_mfma_i32_16x16x64_i8 v[78:81], v[134:137], v[226:229], v[78:81]
	v_mfma_i32_16x16x64_i8 v[74:77], v[168:171], v[226:229], v[74:77]
	s_setprio 0
	s_setprio 1
	v_mfma_i32_16x16x64_i8 v[118:121], v[172:175], v[192:195], v[118:121]
	v_mfma_i32_16x16x64_i8 v[114:117], v[184:187], v[192:195], v[114:117]
	v_mfma_i32_16x16x64_i8 v[102:105], v[172:175], v[206:209], v[102:105]
	v_mfma_i32_16x16x64_i8 v[98:101], v[184:187], v[206:209], v[98:101]
	v_mfma_i32_16x16x64_i8 v[86:89], v[172:175], v[214:217], v[86:89]
	v_mfma_i32_16x16x64_i8 v[82:85], v[184:187], v[214:217], v[82:85]
	v_mfma_i32_16x16x64_i8 v[70:73], v[172:175], v[222:225], v[70:73]
	v_mfma_i32_16x16x64_i8 v[66:69], v[184:187], v[222:225], v[66:69]
	v_mfma_i32_16x16x64_i8 v[118:121], v[176:179], v[202:205], v[118:121]
	v_mfma_i32_16x16x64_i8 v[114:117], v[188:191], v[202:205], v[114:117]
	v_mfma_i32_16x16x64_i8 v[102:105], v[176:179], v[210:213], v[102:105]
	v_mfma_i32_16x16x64_i8 v[98:101], v[188:191], v[210:213], v[98:101]
	v_mfma_i32_16x16x64_i8 v[86:89], v[176:179], v[218:221], v[86:89]
	v_mfma_i32_16x16x64_i8 v[82:85], v[188:191], v[218:221], v[82:85]
	v_mfma_i32_16x16x64_i8 v[70:73], v[176:179], v[226:229], v[70:73]
	v_mfma_i32_16x16x64_i8 v[66:69], v[188:191], v[226:229], v[66:69]
	s_setprio 0
	s_barrier
	s_add_i32 s70, s54, s46
	v_lshl_add_u64 v[160:161], s[42:43], 0, v[140:141]
	s_mov_b32 m0, s70
	ds_read_b128 v[192:195], v183 offset:16384
	ds_read_b128 v[202:205], v183 offset:17408
	ds_read_b128 v[206:209], v183 offset:18432
	ds_read_b128 v[210:213], v183 offset:19456
	ds_read_b128 v[214:217], v183 offset:20480
	ds_read_b128 v[218:221], v183 offset:21504
	ds_read_b128 v[222:225], v183 offset:22528
	ds_read_b128 v[226:229], v183 offset:23552
	global_load_lds_dwordx4 v[160:161], off
	s_add_i32 m0, s70, 0x2000
	s_add_u32 s70, s42, 0x40000
	v_lshl_add_u64 v[198:199], s[42:43], 0, v[144:145]
	s_addc_u32 s71, s43, 0
	s_add_i32 s72, s55, s46
	global_load_lds_dwordx4 v[198:199], off
	v_lshl_add_u64 v[230:231], s[70:71], 0, v[140:141]
	s_mov_b32 m0, s72
	v_lshl_add_u64 v[232:233], s[44:45], 0, v[142:143]
	global_load_lds_dwordx4 v[230:231], off
	v_lshl_add_u64 v[230:231], s[70:71], 0, v[144:145]
	s_add_i32 m0, s72, 0x2000
	s_nop 0
	global_load_lds_dwordx4 v[230:231], off
	v_lshl_add_u64 v[230:231], s[44:45], 0, v[138:139]
	s_mov_b32 m0, s39
	s_nop 0
	global_load_lds_dwordx4 v[230:231], off
	s_mov_b32 m0, s47
	s_nop 0
	global_load_lds_dwordx4 v[232:233], off
	s_waitcnt vmcnt(8)
	s_waitcnt lgkmcnt(0)
	s_setprio 1
	s_waitcnt lgkmcnt(0)
	v_mfma_i32_16x16x64_i8 v[62:65], v[130:133], v[192:195], v[62:65]
	v_mfma_i32_16x16x64_i8 v[58:61], v[164:167], v[192:195], v[58:61]
	v_mfma_i32_16x16x64_i8 v[46:49], v[130:133], v[206:209], v[46:49]
	v_mfma_i32_16x16x64_i8 v[42:45], v[164:167], v[206:209], v[42:45]
	v_mfma_i32_16x16x64_i8 v[30:33], v[130:133], v[214:217], v[30:33]
	v_mfma_i32_16x16x64_i8 v[26:29], v[164:167], v[214:217], v[26:29]
	v_mfma_i32_16x16x64_i8 v[14:17], v[130:133], v[222:225], v[14:17]
	v_mfma_i32_16x16x64_i8 v[10:13], v[164:167], v[222:225], v[10:13]
	s_barrier
; #define PG8_STAGE(bufoff, gbase, voff) do { _Pragma("unroll") for (int _i = 0; _i < 2; ++_i) \
;         __builtin_amdgcn_global_load_lds((const unsigned*)((const char*)(gbase) + (voff)[_i]), (PG8_LAS unsigned*)(lds + (bufoff) + ldsw + _i * 8192), 16, 0, 0); } while (0)
; #define PG8_LDA(dst, b, h) do { _Pragma("unroll") for (int m = 0; m < 4; ++m) _Pragma("unroll") for (int k = 0; k < 2; ++k) dst[m][k] = *(const PG8_LAS bf16x8*)(lds + PG8_SA(b, h) + aoff + m * 2048 + k * 1024); } while (0)
; #define PG8_LDB(dst, b, h) do { _Pragma("unroll") for (int n = 0; n < 2; ++n) _Pragma("unroll") for (int k = 0; k < 2; ++k) dst[n][k] = *(const PG8_LAS bf16x8*)(lds + PG8_SB(b, h) + boff + n * 2048 + k * 1024); } while (0)
; #define PG8_MMA(ai, bj, At, Bt) do { __builtin_amdgcn_s_setprio(1); _Pragma("unroll") for (int m = 0; m < 4; ++m) _Pragma("unroll") for (int n = 0; n < 2; ++n) _Pragma("unroll") for (int k = 0; k < 2; ++k) \
;         acc[ai][bj][m][n] = mma16<I8>(Bt[n][k], At[m][k], acc[ai][bj][m][n]); __builtin_amdgcn_s_setprio(0); } while (0)
; #define PG8_WAIT_V(n) asm volatile("s_waitcnt vmcnt(" #n ")" ::: "memory")
; #define PG8_WAIT_L(n) asm volatile("s_waitcnt lgkmcnt(" #n ")" ::: "memory")
; #define PG8_BAR __builtin_amdgcn_s_barrier()
; #define PG8_SCHED __builtin_amdgcn_sched_barrier(0)
; template <class Epi, class Sched, bool ALIGN_EPI = false, bool SP2 = false, bool I8 = false>
; __device__ __forceinline__ void gemm_phase(PG8_LAS unsigned char* lds, const Gemm g, const Sched& S, const Epi& E) {
;     ...
;             PG8_WAIT_V(8); PG8_WAIT_L(0); PG8_BAR; PG8_MMA(1, 0, At, B0); PG8_MMA(1, 1, At, B1); PG8_BAR; PG8_SCHED;
;             PG8_LDB(B0, 1, 0); PG8_LDB(B1, 1, 1); PG8_SCHED; PG8_LDA(At, 1, 0); PG8_STAGE(PG8_SA(0, 1), a2 + hstep, voffA);
;             PG8_WAIT_V(8); PG8_WAIT_L(0); PG8_BAR; PG8_MMA(0, 0, At, B0); PG8_MMA(0, 1, At, B1); PG8_BAR; PG8_SCHED;
	v_mfma_i32_16x16x64_i8 v[62:65], v[134:137], v[202:205], v[62:65]
	v_mfma_i32_16x16x64_i8 v[58:61], v[168:171], v[202:205], v[58:61]
	v_mfma_i32_16x16x64_i8 v[46:49], v[134:137], v[210:213], v[46:49]
	v_mfma_i32_16x16x64_i8 v[42:45], v[168:171], v[210:213], v[42:45]
	v_mfma_i32_16x16x64_i8 v[30:33], v[134:137], v[218:221], v[30:33]
	v_mfma_i32_16x16x64_i8 v[26:29], v[168:171], v[218:221], v[26:29]
	v_mfma_i32_16x16x64_i8 v[14:17], v[134:137], v[226:229], v[14:17]
	v_mfma_i32_16x16x64_i8 v[10:13], v[168:171], v[226:229], v[10:13]
	s_setprio 0
	s_setprio 1
	v_mfma_i32_16x16x64_i8 v[54:57], v[172:175], v[192:195], v[54:57]
	v_mfma_i32_16x16x64_i8 v[50:53], v[184:187], v[192:195], v[50:53]
	v_mfma_i32_16x16x64_i8 v[38:41], v[172:175], v[206:209], v[38:41]
	v_mfma_i32_16x16x64_i8 v[34:37], v[184:187], v[206:209], v[34:37]
	v_mfma_i32_16x16x64_i8 v[22:25], v[172:175], v[214:217], v[22:25]
	v_mfma_i32_16x16x64_i8 v[18:21], v[184:187], v[214:217], v[18:21]
	v_mfma_i32_16x16x64_i8 v[6:9], v[172:175], v[222:225], v[6:9]
	v_mfma_i32_16x16x64_i8 v[2:5], v[184:187], v[222:225], v[2:5]
	v_mfma_i32_16x16x64_i8 v[54:57], v[176:179], v[202:205], v[54:57]
	v_mfma_i32_16x16x64_i8 v[50:53], v[188:191], v[202:205], v[50:53]
	v_mfma_i32_16x16x64_i8 v[38:41], v[176:179], v[210:213], v[38:41]
	v_mfma_i32_16x16x64_i8 v[34:37], v[188:191], v[210:213], v[34:37]
	v_mfma_i32_16x16x64_i8 v[22:25], v[176:179], v[218:221], v[22:25]
	v_mfma_i32_16x16x64_i8 v[18:21], v[188:191], v[218:221], v[18:21]
	v_mfma_i32_16x16x64_i8 v[6:9], v[176:179], v[226:229], v[6:9]
	v_mfma_i32_16x16x64_i8 v[2:5], v[188:191], v[226:229], v[2:5]
	s_setprio 0
	s_barrier
	s_add_i32 s70, 0, 0x18000
	v_add_u32_e32 v162, s70, v147
	s_add_i32 s71, 0, 0x1c000
	ds_read_b128 v[130:133], v162
	ds_read_b128 v[134:137], v162 offset:1024
	ds_read_b128 v[164:167], v162 offset:2048
	ds_read_b128 v[168:171], v162 offset:3072
	v_add_u32_e32 v162, s71, v147
	ds_read_b128 v[172:175], v162
	ds_read_b128 v[176:179], v162 offset:1024
	ds_read_b128 v[184:187], v162 offset:2048
	ds_read_b128 v[188:191], v162 offset:3072
	s_add_u32 s44, s44, 0x40000
	s_addc_u32 s45, s45, 0
	s_mov_b32 m0, s48
	v_lshl_add_u64 v[234:235], s[44:45], 0, v[138:139]
	ds_read_b128 v[192:195], v183 offset:32768
	ds_read_b128 v[202:205], v183 offset:33792
	ds_read_b128 v[206:209], v183 offset:34816
	ds_read_b128 v[210:213], v183 offset:35840
	ds_read_b128 v[214:217], v183 offset:36864
	ds_read_b128 v[218:221], v183 offset:37888
	ds_read_b128 v[222:225], v183 offset:38912
	ds_read_b128 v[226:229], v183 offset:39936
	global_load_lds_dwordx4 v[234:235], off
	v_lshl_add_u64 v[234:235], s[44:45], 0, v[142:143]
	s_mov_b32 m0, s49
	s_nop 0
	global_load_lds_dwordx4 v[234:235], off
	s_waitcnt vmcnt(8)
	s_waitcnt lgkmcnt(0)
	s_setprio 1
	s_waitcnt lgkmcnt(0)
	v_mfma_i32_16x16x64_i8 v[126:129], v[130:133], v[192:195], v[126:129]
	v_mfma_i32_16x16x64_i8 v[122:125], v[164:167], v[192:195], v[122:125]
	v_mfma_i32_16x16x64_i8 v[110:113], v[130:133], v[206:209], v[110:113]
	v_mfma_i32_16x16x64_i8 v[106:109], v[164:167], v[206:209], v[106:109]
	v_mfma_i32_16x16x64_i8 v[94:97], v[130:133], v[214:217], v[94:97]
	v_mfma_i32_16x16x64_i8 v[90:93], v[164:167], v[214:217], v[90:93]
	v_mfma_i32_16x16x64_i8 v[78:81], v[130:133], v[222:225], v[78:81]
	v_mfma_i32_16x16x64_i8 v[74:77], v[164:167], v[222:225], v[74:77]
	s_barrier
	v_mfma_i32_16x16x64_i8 v[126:129], v[134:137], v[202:205], v[126:129]
	v_mfma_i32_16x16x64_i8 v[122:125], v[168:171], v[202:205], v[122:125]
	v_mfma_i32_16x16x64_i8 v[110:113], v[134:137], v[210:213], v[110:113]
	v_mfma_i32_16x16x64_i8 v[106:109], v[168:171], v[210:213], v[106:109]
	v_mfma_i32_16x16x64_i8 v[94:97], v[134:137], v[218:221], v[94:97]
	v_mfma_i32_16x16x64_i8 v[90:93], v[168:171], v[218:221], v[90:93]
	v_mfma_i32_16x16x64_i8 v[78:81], v[134:137], v[226:229], v[78:81]
	v_mfma_i32_16x16x64_i8 v[74:77], v[168:171], v[226:229], v[74:77]
	s_setprio 0
	s_setprio 1
	v_mfma_i32_16x16x64_i8 v[118:121], v[172:175], v[192:195], v[118:121]
	v_mfma_i32_16x16x64_i8 v[114:117], v[184:187], v[192:195], v[114:117]
	v_mfma_i32_16x16x64_i8 v[102:105], v[172:175], v[206:209], v[102:105]
	v_mfma_i32_16x16x64_i8 v[98:101], v[184:187], v[206:209], v[98:101]
	v_mfma_i32_16x16x64_i8 v[86:89], v[172:175], v[214:217], v[86:89]
	v_mfma_i32_16x16x64_i8 v[82:85], v[184:187], v[214:217], v[82:85]
	v_mfma_i32_16x16x64_i8 v[70:73], v[172:175], v[222:225], v[70:73]
	v_mfma_i32_16x16x64_i8 v[66:69], v[184:187], v[222:225], v[66:69]
	v_mfma_i32_16x16x64_i8 v[118:121], v[176:179], v[202:205], v[118:121]
	v_mfma_i32_16x16x64_i8 v[114:117], v[188:191], v[202:205], v[114:117]
	v_mfma_i32_16x16x64_i8 v[102:105], v[176:179], v[210:213], v[102:105]
	v_mfma_i32_16x16x64_i8 v[98:101], v[188:191], v[210:213], v[98:101]
	v_mfma_i32_16x16x64_i8 v[86:89], v[176:179], v[218:221], v[86:89]
	v_mfma_i32_16x16x64_i8 v[82:85], v[188:191], v[218:221], v[82:85]
	v_mfma_i32_16x16x64_i8 v[70:73], v[176:179], v[226:229], v[70:73]
	v_mfma_i32_16x16x64_i8 v[66:69], v[188:191], v[226:229], v[66:69]
	s_setprio 0
	s_barrier
; #define PG8_STAGE(bufoff, gbase, voff) do { _Pragma("unroll") for (int _i = 0; _i < 2; ++_i) \
;         __builtin_amdgcn_global_load_lds((const unsigned*)((const char*)(gbase) + (voff)[_i]), (PG8_LAS unsigned*)(lds + (bufoff) + ldsw + _i * 8192), 16, 0, 0); } while (0)
; #define PG8_LDA(dst, b, h) do { _Pragma("unroll") for (int m = 0; m < 4; ++m) _Pragma("unroll") for (int k = 0; k < 2; ++k) dst[m][k] = *(const PG8_LAS bf16x8*)(lds + PG8_SA(b, h) + aoff + m * 2048 + k * 1024); } while (0)
; #define PG8_MMA(ai, bj, At, Bt) do { __builtin_amdgcn_s_setprio(1); _Pragma("unroll") for (int m = 0; m < 4; ++m) _Pragma("unroll") for (int n = 0; n < 2; ++n) _Pragma("unroll") for (int k = 0; k < 2; ++k) \
;         acc[ai][bj][m][n] = mma16<I8>(Bt[n][k], At[m][k], acc[ai][bj][m][n]); __builtin_amdgcn_s_setprio(0); } while (0)
; #define PG8_WAIT_V(n) asm volatile("s_waitcnt vmcnt(" #n ")" ::: "memory")
; #define PG8_WAIT_L(n) asm volatile("s_waitcnt lgkmcnt(" #n ")" ::: "memory")
; #define PG8_BAR __builtin_amdgcn_s_barrier()
; #define PG8_SCHED __builtin_amdgcn_sched_barrier(0)
; template <class Epi, class Sched, bool ALIGN_EPI = false, bool SP2 = false, bool I8 = false>
; __device__ __forceinline__ void gemm_phase(PG8_LAS unsigned char* lds, const Gemm g, const Sched& S, const Epi& E) {
;     ...
;         for (int t = 0; t < nt; t += 2) {
;     ...
;             PG8_LDA(At, 1, 1); PG8_STAGE(PG8_SB(1, 0), b3, voffB); PG8_STAGE(PG8_SB(1, 1), b3 + hstep, voffB); PG8_STAGE(PG8_SA(1, 0), a3, voffA);
;             PG8_WAIT_V(8); PG8_WAIT_L(0); PG8_BAR; PG8_MMA(1, 0, At, B0); PG8_MMA(1, 1, At, B1); PG8_BAR; PG8_SCHED;
	s_add_i32 s44, s70, s46
	v_lshl_add_u64 v[160:161], v[160:161], 0, s[14:15]
	s_mov_b32 m0, s44
	ds_read_b128 v[192:195], v183 offset:49152
	ds_read_b128 v[202:205], v183 offset:50176
	ds_read_b128 v[206:209], v183 offset:51200
	ds_read_b128 v[210:213], v183 offset:52224
	ds_read_b128 v[214:217], v183 offset:53248
	ds_read_b128 v[218:221], v183 offset:54272
	ds_read_b128 v[222:225], v183 offset:55296
	ds_read_b128 v[226:229], v183 offset:56320
	global_load_lds_dwordx4 v[160:161], off
	s_add_i32 m0, s44, 0x2000
	s_add_u32 s42, s42, 0x40080
	v_lshl_add_u64 v[160:161], v[198:199], 0, s[14:15]
	s_addc_u32 s43, s43, 0
	s_add_i32 s44, s71, s46
	global_load_lds_dwordx4 v[160:161], off
	v_lshl_add_u64 v[160:161], s[42:43], 0, v[140:141]
	s_mov_b32 m0, s44
	s_nop 0
	global_load_lds_dwordx4 v[160:161], off
	v_lshl_add_u64 v[160:161], s[42:43], 0, v[144:145]
	s_add_i32 m0, s44, 0x2000
	s_nop 0
	global_load_lds_dwordx4 v[160:161], off
	v_lshl_add_u64 v[160:161], v[230:231], 0, s[14:15]
	s_mov_b32 m0, s51
	s_nop 0
	global_load_lds_dwordx4 v[160:161], off
	v_lshl_add_u64 v[160:161], v[232:233], 0, s[14:15]
	s_mov_b32 m0, s52
	s_nop 0
	global_load_lds_dwordx4 v[160:161], off
	s_waitcnt vmcnt(8)
	s_waitcnt lgkmcnt(0)
	s_setprio 1
	s_waitcnt lgkmcnt(0)
	v_mfma_i32_16x16x64_i8 v[62:65], v[130:133], v[192:195], v[62:65]
	v_mfma_i32_16x16x64_i8 v[58:61], v[164:167], v[192:195], v[58:61]
	v_mfma_i32_16x16x64_i8 v[46:49], v[130:133], v[206:209], v[46:49]
	v_mfma_i32_16x16x64_i8 v[42:45], v[164:167], v[206:209], v[42:45]
	v_mfma_i32_16x16x64_i8 v[30:33], v[130:133], v[214:217], v[30:33]
	v_mfma_i32_16x16x64_i8 v[26:29], v[164:167], v[214:217], v[26:29]
	v_mfma_i32_16x16x64_i8 v[14:17], v[130:133], v[222:225], v[14:17]
	v_mfma_i32_16x16x64_i8 v[10:13], v[164:167], v[222:225], v[10:13]
	s_barrier
	v_mfma_i32_16x16x64_i8 v[62:65], v[134:137], v[202:205], v[62:65]
	v_mfma_i32_16x16x64_i8 v[58:61], v[168:171], v[202:205], v[58:61]
	v_mfma_i32_16x16x64_i8 v[46:49], v[134:137], v[210:213], v[46:49]
	v_mfma_i32_16x16x64_i8 v[42:45], v[168:171], v[210:213], v[42:45]
	v_mfma_i32_16x16x64_i8 v[30:33], v[134:137], v[218:221], v[30:33]
	v_mfma_i32_16x16x64_i8 v[26:29], v[168:171], v[218:221], v[26:29]
	v_mfma_i32_16x16x64_i8 v[14:17], v[134:137], v[226:229], v[14:17]
	v_mfma_i32_16x16x64_i8 v[10:13], v[168:171], v[226:229], v[10:13]
	s_setprio 0
	s_setprio 1
	v_mfma_i32_16x16x64_i8 v[54:57], v[172:175], v[192:195], v[54:57]
	v_mfma_i32_16x16x64_i8 v[50:53], v[184:187], v[192:195], v[50:53]
	v_mfma_i32_16x16x64_i8 v[38:41], v[172:175], v[206:209], v[38:41]
	v_mfma_i32_16x16x64_i8 v[34:37], v[184:187], v[206:209], v[34:37]
	v_mfma_i32_16x16x64_i8 v[22:25], v[172:175], v[214:217], v[22:25]
	v_mfma_i32_16x16x64_i8 v[18:21], v[184:187], v[214:217], v[18:21]
	v_mfma_i32_16x16x64_i8 v[6:9], v[172:175], v[222:225], v[6:9]
	v_mfma_i32_16x16x64_i8 v[2:5], v[184:187], v[222:225], v[2:5]
	v_mfma_i32_16x16x64_i8 v[54:57], v[176:179], v[202:205], v[54:57]
	v_mfma_i32_16x16x64_i8 v[50:53], v[188:191], v[202:205], v[50:53]
	v_mfma_i32_16x16x64_i8 v[38:41], v[176:179], v[210:213], v[38:41]
	v_mfma_i32_16x16x64_i8 v[34:37], v[188:191], v[210:213], v[34:37]
	v_mfma_i32_16x16x64_i8 v[22:25], v[176:179], v[218:221], v[22:25]
	v_mfma_i32_16x16x64_i8 v[18:21], v[188:191], v[218:221], v[18:21]
	v_mfma_i32_16x16x64_i8 v[6:9], v[176:179], v[226:229], v[6:9]
	v_mfma_i32_16x16x64_i8 v[2:5], v[188:191], v[226:229], v[2:5]
	s_setprio 0
	s_barrier
	s_add_i32 s63, s63, 2
	s_add_u32 s40, s40, 0x100
	s_addc_u32 s41, s41, 0
	s_add_u32 s59, s59, 0x100
	s_addc_u32 s62, s62, 0
	s_cmp_gt_u32 s63, 13
	s_cbranch_scc0 .LBB0_974
	s_and_b64 vcc, exec, s[16:17]
	s_cbranch_vccz .LBB0_977
	s_barrier

; #define PG8_STAGE(bufoff, gbase, voff) do { _Pragma("unroll") for (int _i = 0; _i < 2; ++_i) \
;         __builtin_amdgcn_global_load_lds((const unsigned*)((const char*)(gbase) + (voff)[_i]), (PG8_LAS unsigned*)(lds + (bufoff) + ldsw + _i * 8192), 16, 0, 0); } while (0)
; #define PG8_LDA(dst, b, h) do { _Pragma("unroll") for (int m = 0; m < 4; ++m) _Pragma("unroll") for (int k = 0; k < 2; ++k) dst[m][k] = *(const PG8_LAS bf16x8*)(lds + PG8_SA(b, h) + aoff + m * 2048 + k * 1024); } while (0)
; #define PG8_LDB(dst, b, h) do { _Pragma("unroll") for (int n = 0; n < 2; ++n) _Pragma("unroll") for (int k = 0; k < 2; ++k) dst[n][k] = *(const PG8_LAS bf16x8*)(lds + PG8_SB(b, h) + boff + n * 2048 + k * 1024); } while (0)
; #define PG8_MMA(ai, bj, At, Bt) do { __builtin_amdgcn_s_setprio(1); _Pragma("unroll") for (int m = 0; m < 4; ++m) _Pragma("unroll") for (int n = 0; n < 2; ++n) _Pragma("unroll") for (int k = 0; k < 2; ++k) \
;         acc[ai][bj][m][n] = mma16<I8>(Bt[n][k], At[m][k], acc[ai][bj][m][n]); __builtin_amdgcn_s_setprio(0); } while (0)
; #define PG8_WAIT_V(n) asm volatile("s_waitcnt vmcnt(" #n ")" ::: "memory")
; #define PG8_WAIT_L(n) asm volatile("s_waitcnt lgkmcnt(" #n ")" ::: "memory")
; #define PG8_BAR __builtin_amdgcn_s_barrier()
; #define PG8_SCHED __builtin_amdgcn_sched_barrier(0)
; template <class Epi, class Sched, bool ALIGN_EPI = false, bool SP2 = false, bool I8 = false>
; __device__ __forceinline__ void gemm_phase(PG8_LAS unsigned char* lds, const Gemm g, const Sched& S, const Epi& E) {
;     ...
;             PG8_LDB(B0, 0, 0); PG8_LDB(B1, 0, 1); PG8_SCHED; PG8_LDA(At, 0, 0); PG8_STAGE(PG8_SA(1, 1), a1 + hstep, voffA);
;             PG8_WAIT_V(8); PG8_WAIT_L(0); PG8_BAR; PG8_MMA(0, 0, At, B0); PG8_MMA(0, 1, At, B1); PG8_BAR; PG8_SCHED;
;             PG8_LDA(At, 0, 1); PG8_STAGE(PG8_SB(0, 0), b2, voffB); PG8_STAGE(PG8_SB(0, 1), b2 + hstep, voffB); PG8_STAGE(PG8_SA(0, 0), a2, voffA);
;             PG8_WAIT_V(8); PG8_WAIT_L(0); PG8_BAR; PG8_MMA(1, 0, At, B0); PG8_MMA(1, 1, At, B1); PG8_BAR; PG8_SCHED;
.LBB0_1112:
	ds_read_b128 v[34:37], v196
	ds_read_b128 v[38:41], v196 offset:1024
	ds_read_b128 v[50:53], v196 offset:2048
	ds_read_b128 v[54:57], v196 offset:3072
	ds_read_b128 v[168:171], v198
	ds_read_b128 v[172:175], v198 offset:1024
	ds_read_b128 v[176:179], v198 offset:2048
	ds_read_b128 v[180:183], v198 offset:3072
	s_add_u32 s48, s46, 0xfffc0080
	s_addc_u32 s49, s47, -1
	s_cmp_eq_u32 s62, 12
	s_cselect_b32 s51, s5, s49
	s_cselect_b32 s50, s33, s48
	s_cselect_b32 s49, s39, s59
	s_cselect_b32 s48, s41, s58
	v_lshl_add_u64 v[222:223], s[46:47], 0, v[160:161]
	s_add_i32 m0, s3, 0xc000
	ds_read_b128 v[184:187], v199
	ds_read_b128 v[188:191], v199 offset:1024
	ds_read_b128 v[192:195], v199 offset:2048
	ds_read_b128 v[202:205], v199 offset:3072
	ds_read_b128 v[206:209], v199 offset:4096
	ds_read_b128 v[210:213], v199 offset:5120
	ds_read_b128 v[214:217], v199 offset:6144
	ds_read_b128 v[218:221], v199 offset:7168
	global_load_lds_dwordx4 v[222:223], off
	v_lshl_add_u64 v[222:223], s[46:47], 0, v[162:163]
	s_add_i32 m0, s3, 0xe000
	s_nop 0
	global_load_lds_dwordx4 v[222:223], off
	s_waitcnt vmcnt(8)
	s_waitcnt lgkmcnt(0)
	s_setprio 1
	s_waitcnt lgkmcnt(0)
	v_mfma_i32_16x16x64_i8 v[142:145], v[34:37], v[184:187], v[142:145]
	v_mfma_i32_16x16x64_i8 v[138:141], v[50:53], v[184:187], v[138:141]
	v_mfma_i32_16x16x64_i8 v[126:129], v[34:37], v[192:195], v[126:129]
	v_mfma_i32_16x16x64_i8 v[122:125], v[50:53], v[192:195], v[122:125]
	v_mfma_i32_16x16x64_i8 v[110:113], v[34:37], v[206:209], v[110:113]
	v_mfma_i32_16x16x64_i8 v[106:109], v[50:53], v[206:209], v[106:109]
	v_mfma_i32_16x16x64_i8 v[94:97], v[34:37], v[214:217], v[94:97]
	v_mfma_i32_16x16x64_i8 v[90:93], v[50:53], v[214:217], v[90:93]
	s_barrier
	v_mfma_i32_16x16x64_i8 v[142:145], v[38:41], v[188:191], v[142:145]
	v_mfma_i32_16x16x64_i8 v[138:141], v[54:57], v[188:191], v[138:141]
	v_mfma_i32_16x16x64_i8 v[126:129], v[38:41], v[202:205], v[126:129]
	v_mfma_i32_16x16x64_i8 v[122:125], v[54:57], v[202:205], v[122:125]
	v_mfma_i32_16x16x64_i8 v[110:113], v[38:41], v[210:213], v[110:113]
	v_mfma_i32_16x16x64_i8 v[106:109], v[54:57], v[210:213], v[106:109]
	v_mfma_i32_16x16x64_i8 v[94:97], v[38:41], v[218:221], v[94:97]
	v_mfma_i32_16x16x64_i8 v[90:93], v[54:57], v[218:221], v[90:93]
	s_setprio 0
	s_setprio 1
	v_mfma_i32_16x16x64_i8 v[134:137], v[168:171], v[184:187], v[134:137]
	v_mfma_i32_16x16x64_i8 v[130:133], v[176:179], v[184:187], v[130:133]
	v_mfma_i32_16x16x64_i8 v[118:121], v[168:171], v[192:195], v[118:121]
	v_mfma_i32_16x16x64_i8 v[114:117], v[176:179], v[192:195], v[114:117]
	v_mfma_i32_16x16x64_i8 v[102:105], v[168:171], v[206:209], v[102:105]
	v_mfma_i32_16x16x64_i8 v[98:101], v[176:179], v[206:209], v[98:101]
	v_mfma_i32_16x16x64_i8 v[86:89], v[168:171], v[214:217], v[86:89]
	v_mfma_i32_16x16x64_i8 v[82:85], v[176:179], v[214:217], v[82:85]
	v_mfma_i32_16x16x64_i8 v[134:137], v[172:175], v[188:191], v[134:137]
	v_mfma_i32_16x16x64_i8 v[130:133], v[180:183], v[188:191], v[130:133]
	v_mfma_i32_16x16x64_i8 v[118:121], v[172:175], v[202:205], v[118:121]
	v_mfma_i32_16x16x64_i8 v[114:117], v[180:183], v[202:205], v[114:117]
	v_mfma_i32_16x16x64_i8 v[102:105], v[172:175], v[210:213], v[102:105]
	v_mfma_i32_16x16x64_i8 v[98:101], v[180:183], v[210:213], v[98:101]
	v_mfma_i32_16x16x64_i8 v[86:89], v[172:175], v[218:221], v[86:89]
	v_mfma_i32_16x16x64_i8 v[82:85], v[180:183], v[218:221], v[82:85]
	s_setprio 0
	s_barrier
	s_add_i32 s63, s54, s15
	v_lshl_add_u64 v[222:223], s[48:49], 0, v[154:155]
	s_mov_b32 m0, s63
	ds_read_b128 v[184:187], v199 offset:16384
	ds_read_b128 v[188:191], v199 offset:17408
	ds_read_b128 v[192:195], v199 offset:18432
	ds_read_b128 v[202:205], v199 offset:19456
	ds_read_b128 v[206:209], v199 offset:20480
	ds_read_b128 v[210:213], v199 offset:21504
	ds_read_b128 v[214:217], v199 offset:22528
	ds_read_b128 v[218:221], v199 offset:23552
	global_load_lds_dwordx4 v[222:223], off
	s_add_i32 m0, s63, 0x2000
	s_add_u32 s70, s48, 0x40000
	v_lshl_add_u64 v[224:225], s[48:49], 0, v[158:159]
	s_addc_u32 s71, s49, 0
	s_add_i32 s63, s55, s15
	global_load_lds_dwordx4 v[224:225], off
	v_lshl_add_u64 v[226:227], s[70:71], 0, v[154:155]
	s_mov_b32 m0, s63
	v_lshl_add_u64 v[228:229], s[50:51], 0, v[156:157]
	global_load_lds_dwordx4 v[226:227], off
	v_lshl_add_u64 v[226:227], s[70:71], 0, v[158:159]
	s_add_i32 m0, s63, 0x2000
	s_nop 0
	global_load_lds_dwordx4 v[226:227], off
	v_lshl_add_u64 v[226:227], s[50:51], 0, v[152:153]
	s_mov_b32 m0, s3
	s_nop 0
	global_load_lds_dwordx4 v[226:227], off
	s_mov_b32 m0, s17
	s_nop 0
	global_load_lds_dwordx4 v[228:229], off
	s_waitcnt vmcnt(8)
	s_waitcnt lgkmcnt(0)
	s_setprio 1
	s_waitcnt lgkmcnt(0)
	v_mfma_i32_16x16x64_i8 v[78:81], v[34:37], v[184:187], v[78:81]
	v_mfma_i32_16x16x64_i8 v[74:77], v[50:53], v[184:187], v[74:77]
	v_mfma_i32_16x16x64_i8 v[62:65], v[34:37], v[192:195], v[62:65]
	v_mfma_i32_16x16x64_i8 v[58:61], v[50:53], v[192:195], v[58:61]
	v_mfma_i32_16x16x64_i8 v[30:33], v[34:37], v[206:209], v[30:33]
	v_mfma_i32_16x16x64_i8 v[26:29], v[50:53], v[206:209], v[26:29]
	v_mfma_i32_16x16x64_i8 v[14:17], v[34:37], v[214:217], v[14:17]
	v_mfma_i32_16x16x64_i8 v[10:13], v[50:53], v[214:217], v[10:13]
	s_barrier
; #define PG8_STAGE(bufoff, gbase, voff) do { _Pragma("unroll") for (int _i = 0; _i < 2; ++_i) \
;         __builtin_amdgcn_global_load_lds((const unsigned*)((const char*)(gbase) + (voff)[_i]), (PG8_LAS unsigned*)(lds + (bufoff) + ldsw + _i * 8192), 16, 0, 0); } while (0)
; #define PG8_LDA(dst, b, h) do { _Pragma("unroll") for (int m = 0; m < 4; ++m) _Pragma("unroll") for (int k = 0; k < 2; ++k) dst[m][k] = *(const PG8_LAS bf16x8*)(lds + PG8_SA(b, h) + aoff + m * 2048 + k * 1024); } while (0)
; #define PG8_LDB(dst, b, h) do { _Pragma("unroll") for (int n = 0; n < 2; ++n) _Pragma("unroll") for (int k = 0; k < 2; ++k) dst[n][k] = *(const PG8_LAS bf16x8*)(lds + PG8_SB(b, h) + boff + n * 2048 + k * 1024); } while (0)
; #define PG8_MMA(ai, bj, At, Bt) do { __builtin_amdgcn_s_setprio(1); _Pragma("unroll") for (int m = 0; m < 4; ++m) _Pragma("unroll") for (int n = 0; n < 2; ++n) _Pragma("unroll") for (int k = 0; k < 2; ++k) \
;         acc[ai][bj][m][n] = mma16<I8>(Bt[n][k], At[m][k], acc[ai][bj][m][n]); __builtin_amdgcn_s_setprio(0); } while (0)
; #define PG8_WAIT_V(n) asm volatile("s_waitcnt vmcnt(" #n ")" ::: "memory")
; #define PG8_WAIT_L(n) asm volatile("s_waitcnt lgkmcnt(" #n ")" ::: "memory")
; #define PG8_BAR __builtin_amdgcn_s_barrier()
; #define PG8_SCHED __builtin_amdgcn_sched_barrier(0)
; template <class Epi, class Sched, bool ALIGN_EPI = false, bool SP2 = false, bool I8 = false>
; __device__ __forceinline__ void gemm_phase(PG8_LAS unsigned char* lds, const Gemm g, const Sched& S, const Epi& E) {
;     ...
;             PG8_WAIT_V(8); PG8_WAIT_L(0); PG8_BAR; PG8_MMA(1, 0, At, B0); PG8_MMA(1, 1, At, B1); PG8_BAR; PG8_SCHED;
;             PG8_LDB(B0, 1, 0); PG8_LDB(B1, 1, 1); PG8_SCHED; PG8_LDA(At, 1, 0); PG8_STAGE(PG8_SA(0, 1), a2 + hstep, voffA);
;             PG8_WAIT_V(8); PG8_WAIT_L(0); PG8_BAR; PG8_MMA(0, 0, At, B0); PG8_MMA(0, 1, At, B1); PG8_BAR; PG8_SCHED;
	v_mfma_i32_16x16x64_i8 v[78:81], v[38:41], v[188:191], v[78:81]
	v_mfma_i32_16x16x64_i8 v[74:77], v[54:57], v[188:191], v[74:77]
	v_mfma_i32_16x16x64_i8 v[62:65], v[38:41], v[202:205], v[62:65]
	v_mfma_i32_16x16x64_i8 v[58:61], v[54:57], v[202:205], v[58:61]
	v_mfma_i32_16x16x64_i8 v[30:33], v[38:41], v[210:213], v[30:33]
	v_mfma_i32_16x16x64_i8 v[26:29], v[54:57], v[210:213], v[26:29]
	v_mfma_i32_16x16x64_i8 v[14:17], v[38:41], v[218:221], v[14:17]
	v_mfma_i32_16x16x64_i8 v[10:13], v[54:57], v[218:221], v[10:13]
	s_setprio 0
	s_setprio 1
	v_mfma_i32_16x16x64_i8 v[46:49], v[168:171], v[192:195], v[46:49]
	v_mfma_i32_16x16x64_i8 v[42:45], v[176:179], v[192:195], v[42:45]
	v_mfma_i32_16x16x64_i8 v[22:25], v[168:171], v[206:209], v[22:25]
	v_mfma_i32_16x16x64_i8 v[18:21], v[176:179], v[206:209], v[18:21]
	v_mfma_i32_16x16x64_i8 v[6:9], v[168:171], v[214:217], v[6:9]
	v_mfma_i32_16x16x64_i8 v[2:5], v[176:179], v[214:217], v[2:5]
	v_mfma_i32_16x16x64_i8 v[34:37], v[168:171], v[184:187], v[70:73]
	v_mfma_i32_16x16x64_i8 v[38:41], v[176:179], v[184:187], v[66:69]
	v_mfma_i32_16x16x64_i8 v[46:49], v[172:175], v[202:205], v[46:49]
	v_mfma_i32_16x16x64_i8 v[42:45], v[180:183], v[202:205], v[42:45]
	v_mfma_i32_16x16x64_i8 v[22:25], v[172:175], v[210:213], v[22:25]
	v_mfma_i32_16x16x64_i8 v[18:21], v[180:183], v[210:213], v[18:21]
	v_mfma_i32_16x16x64_i8 v[6:9], v[172:175], v[218:221], v[6:9]
	v_mfma_i32_16x16x64_i8 v[2:5], v[180:183], v[218:221], v[2:5]
	v_mfma_i32_16x16x64_i8 v[34:37], v[172:175], v[188:191], v[34:37]
	v_mfma_i32_16x16x64_i8 v[38:41], v[180:183], v[188:191], v[38:41]
	s_setprio 0
	s_barrier
	s_add_i32 s63, 0, 0x18000
	s_add_i32 s70, 0, 0x1c000
	v_add_u32_e32 v70, s63, v147
	v_add_u32_e32 v180, s70, v147
	ds_read_b128 v[50:53], v70
	ds_read_b128 v[54:57], v70 offset:1024
	ds_read_b128 v[66:69], v70 offset:2048
	ds_read_b128 v[70:73], v70 offset:3072
	ds_read_b128 v[168:171], v180
	ds_read_b128 v[172:175], v180 offset:1024
	ds_read_b128 v[176:179], v180 offset:2048
	ds_read_b128 v[180:183], v180 offset:3072
	s_add_u32 s50, s50, 0x40000
	s_addc_u32 s51, s51, 0
	s_mov_b32 m0, s25
	v_lshl_add_u64 v[230:231], s[50:51], 0, v[152:153]
	ds_read_b128 v[184:187], v199 offset:32768
	ds_read_b128 v[188:191], v199 offset:33792
	ds_read_b128 v[192:195], v199 offset:34816
	ds_read_b128 v[202:205], v199 offset:35840
	ds_read_b128 v[206:209], v199 offset:36864
	ds_read_b128 v[210:213], v199 offset:37888
	ds_read_b128 v[214:217], v199 offset:38912
	ds_read_b128 v[218:221], v199 offset:39936
	global_load_lds_dwordx4 v[230:231], off
	v_lshl_add_u64 v[230:231], s[50:51], 0, v[156:157]
	s_mov_b32 m0, s27
	s_nop 0
	global_load_lds_dwordx4 v[230:231], off
	s_waitcnt vmcnt(8)
	s_waitcnt lgkmcnt(0)
	s_setprio 1
	s_waitcnt lgkmcnt(0)
	v_mfma_i32_16x16x64_i8 v[142:145], v[50:53], v[184:187], v[142:145]
	v_mfma_i32_16x16x64_i8 v[138:141], v[66:69], v[184:187], v[138:141]
	v_mfma_i32_16x16x64_i8 v[126:129], v[50:53], v[192:195], v[126:129]
	v_mfma_i32_16x16x64_i8 v[122:125], v[66:69], v[192:195], v[122:125]
	v_mfma_i32_16x16x64_i8 v[110:113], v[50:53], v[206:209], v[110:113]
	v_mfma_i32_16x16x64_i8 v[106:109], v[66:69], v[206:209], v[106:109]
	v_mfma_i32_16x16x64_i8 v[94:97], v[50:53], v[214:217], v[94:97]
	v_mfma_i32_16x16x64_i8 v[90:93], v[66:69], v[214:217], v[90:93]
	s_barrier
	v_mfma_i32_16x16x64_i8 v[142:145], v[54:57], v[188:191], v[142:145]
	v_mfma_i32_16x16x64_i8 v[138:141], v[70:73], v[188:191], v[138:141]
	v_mfma_i32_16x16x64_i8 v[126:129], v[54:57], v[202:205], v[126:129]
	v_mfma_i32_16x16x64_i8 v[122:125], v[70:73], v[202:205], v[122:125]
	v_mfma_i32_16x16x64_i8 v[110:113], v[54:57], v[210:213], v[110:113]
	v_mfma_i32_16x16x64_i8 v[106:109], v[70:73], v[210:213], v[106:109]
	v_mfma_i32_16x16x64_i8 v[94:97], v[54:57], v[218:221], v[94:97]
	v_mfma_i32_16x16x64_i8 v[90:93], v[70:73], v[218:221], v[90:93]
	s_setprio 0
	s_setprio 1
	v_mfma_i32_16x16x64_i8 v[134:137], v[168:171], v[184:187], v[134:137]
	v_mfma_i32_16x16x64_i8 v[130:133], v[176:179], v[184:187], v[130:133]
	v_mfma_i32_16x16x64_i8 v[118:121], v[168:171], v[192:195], v[118:121]
	v_mfma_i32_16x16x64_i8 v[114:117], v[176:179], v[192:195], v[114:117]
	v_mfma_i32_16x16x64_i8 v[102:105], v[168:171], v[206:209], v[102:105]
	v_mfma_i32_16x16x64_i8 v[98:101], v[176:179], v[206:209], v[98:101]
	v_mfma_i32_16x16x64_i8 v[86:89], v[168:171], v[214:217], v[86:89]
	v_mfma_i32_16x16x64_i8 v[82:85], v[176:179], v[214:217], v[82:85]
	v_mfma_i32_16x16x64_i8 v[134:137], v[172:175], v[188:191], v[134:137]
	v_mfma_i32_16x16x64_i8 v[130:133], v[180:183], v[188:191], v[130:133]
	v_mfma_i32_16x16x64_i8 v[118:121], v[172:175], v[202:205], v[118:121]
	v_mfma_i32_16x16x64_i8 v[114:117], v[180:183], v[202:205], v[114:117]
	v_mfma_i32_16x16x64_i8 v[102:105], v[172:175], v[210:213], v[102:105]
	v_mfma_i32_16x16x64_i8 v[98:101], v[180:183], v[210:213], v[98:101]
	v_mfma_i32_16x16x64_i8 v[86:89], v[172:175], v[218:221], v[86:89]
	v_mfma_i32_16x16x64_i8 v[82:85], v[180:183], v[218:221], v[82:85]
	s_setprio 0
	s_barrier
; #define PG8_STAGE(bufoff, gbase, voff) do { _Pragma("unroll") for (int _i = 0; _i < 2; ++_i) \
;         __builtin_amdgcn_global_load_lds((const unsigned*)((const char*)(gbase) + (voff)[_i]), (PG8_LAS unsigned*)(lds + (bufoff) + ldsw + _i * 8192), 16, 0, 0); } while (0)
; #define PG8_LDA(dst, b, h) do { _Pragma("unroll") for (int m = 0; m < 4; ++m) _Pragma("unroll") for (int k = 0; k < 2; ++k) dst[m][k] = *(const PG8_LAS bf16x8*)(lds + PG8_SA(b, h) + aoff + m * 2048 + k * 1024); } while (0)
; #define PG8_MMA(ai, bj, At, Bt) do { __builtin_amdgcn_s_setprio(1); _Pragma("unroll") for (int m = 0; m < 4; ++m) _Pragma("unroll") for (int n = 0; n < 2; ++n) _Pragma("unroll") for (int k = 0; k < 2; ++k) \
;         acc[ai][bj][m][n] = mma16<I8>(Bt[n][k], At[m][k], acc[ai][bj][m][n]); __builtin_amdgcn_s_setprio(0); } while (0)
; #define PG8_WAIT_V(n) asm volatile("s_waitcnt vmcnt(" #n ")" ::: "memory")
; #define PG8_WAIT_L(n) asm volatile("s_waitcnt lgkmcnt(" #n ")" ::: "memory")
; #define PG8_BAR __builtin_amdgcn_s_barrier()
; #define PG8_SCHED __builtin_amdgcn_sched_barrier(0)
; template <class Epi, class Sched, bool ALIGN_EPI = false, bool SP2 = false, bool I8 = false>
; __device__ __forceinline__ void gemm_phase(PG8_LAS unsigned char* lds, const Gemm g, const Sched& S, const Epi& E) {
;     ...
;         for (int t = 0; t < nt; t += 2) {
;     ...
;             PG8_LDA(At, 1, 1); PG8_STAGE(PG8_SB(1, 0), b3, voffB); PG8_STAGE(PG8_SB(1, 1), b3 + hstep, voffB); PG8_STAGE(PG8_SA(1, 0), a3, voffA);
;             PG8_WAIT_V(8); PG8_WAIT_L(0); PG8_BAR; PG8_MMA(1, 0, At, B0); PG8_MMA(1, 1, At, B1); PG8_BAR; PG8_SCHED;
	s_add_i32 s50, s63, s15
	v_lshl_add_u64 v[222:223], v[222:223], 0, s[10:11]
	s_mov_b32 m0, s50
	ds_read_b128 v[184:187], v199 offset:49152
	ds_read_b128 v[188:191], v199 offset:50176
	ds_read_b128 v[192:195], v199 offset:51200
	ds_read_b128 v[202:205], v199 offset:52224
	ds_read_b128 v[206:209], v199 offset:53248
	ds_read_b128 v[210:213], v199 offset:54272
	ds_read_b128 v[214:217], v199 offset:55296
	ds_read_b128 v[218:221], v199 offset:56320
	global_load_lds_dwordx4 v[222:223], off
	s_add_i32 m0, s50, 0x2000
	s_add_u32 s48, s48, 0x40080
	v_lshl_add_u64 v[222:223], v[224:225], 0, s[10:11]
	s_addc_u32 s49, s49, 0
	s_add_i32 s50, s70, s15
	global_load_lds_dwordx4 v[222:223], off
	v_lshl_add_u64 v[222:223], s[48:49], 0, v[154:155]
	s_mov_b32 m0, s50
	s_nop 0
	global_load_lds_dwordx4 v[222:223], off
	v_lshl_add_u64 v[222:223], s[48:49], 0, v[158:159]
	s_add_i32 m0, s50, 0x2000
	s_nop 0
	global_load_lds_dwordx4 v[222:223], off
	v_lshl_add_u64 v[222:223], v[226:227], 0, s[10:11]
	s_mov_b32 m0, s31
	s_nop 0
	global_load_lds_dwordx4 v[222:223], off
	v_lshl_add_u64 v[222:223], v[228:229], 0, s[10:11]
	s_mov_b32 m0, s35
	s_nop 0
	global_load_lds_dwordx4 v[222:223], off
	s_waitcnt vmcnt(8)
	s_waitcnt lgkmcnt(0)
	s_setprio 1
	s_waitcnt lgkmcnt(0)
	v_mfma_i32_16x16x64_i8 v[78:81], v[50:53], v[184:187], v[78:81]
	v_mfma_i32_16x16x64_i8 v[74:77], v[66:69], v[184:187], v[74:77]
	v_mfma_i32_16x16x64_i8 v[62:65], v[50:53], v[192:195], v[62:65]
	v_mfma_i32_16x16x64_i8 v[58:61], v[66:69], v[192:195], v[58:61]
	v_mfma_i32_16x16x64_i8 v[30:33], v[50:53], v[206:209], v[30:33]
	v_mfma_i32_16x16x64_i8 v[26:29], v[66:69], v[206:209], v[26:29]
	v_mfma_i32_16x16x64_i8 v[14:17], v[50:53], v[214:217], v[14:17]
	v_mfma_i32_16x16x64_i8 v[10:13], v[66:69], v[214:217], v[10:13]
	s_barrier
	v_mfma_i32_16x16x64_i8 v[78:81], v[54:57], v[188:191], v[78:81]
	v_mfma_i32_16x16x64_i8 v[74:77], v[70:73], v[188:191], v[74:77]
	v_mfma_i32_16x16x64_i8 v[62:65], v[54:57], v[202:205], v[62:65]
	v_mfma_i32_16x16x64_i8 v[58:61], v[70:73], v[202:205], v[58:61]
	v_mfma_i32_16x16x64_i8 v[30:33], v[54:57], v[210:213], v[30:33]
	v_mfma_i32_16x16x64_i8 v[26:29], v[70:73], v[210:213], v[26:29]
	v_mfma_i32_16x16x64_i8 v[14:17], v[54:57], v[218:221], v[14:17]
	v_mfma_i32_16x16x64_i8 v[10:13], v[70:73], v[218:221], v[10:13]
	s_setprio 0
	s_setprio 1
	v_mfma_i32_16x16x64_i8 v[34:37], v[168:171], v[184:187], v[34:37]
	v_mfma_i32_16x16x64_i8 v[70:73], v[172:175], v[188:191], v[34:37]
	v_mfma_i32_16x16x64_i8 v[34:37], v[176:179], v[184:187], v[38:41]
	v_mfma_i32_16x16x64_i8 v[66:69], v[180:183], v[188:191], v[34:37]
	v_mfma_i32_16x16x64_i8 v[34:37], v[168:171], v[192:195], v[46:49]
	v_mfma_i32_16x16x64_i8 v[46:49], v[172:175], v[202:205], v[34:37]
	v_mfma_i32_16x16x64_i8 v[34:37], v[176:179], v[192:195], v[42:45]
	v_mfma_i32_16x16x64_i8 v[22:25], v[168:171], v[206:209], v[22:25]
	v_mfma_i32_16x16x64_i8 v[18:21], v[176:179], v[206:209], v[18:21]
	v_mfma_i32_16x16x64_i8 v[6:9], v[168:171], v[214:217], v[6:9]
	v_mfma_i32_16x16x64_i8 v[2:5], v[176:179], v[214:217], v[2:5]
	v_mfma_i32_16x16x64_i8 v[42:45], v[180:183], v[202:205], v[34:37]
	v_mfma_i32_16x16x64_i8 v[22:25], v[172:175], v[210:213], v[22:25]
	v_mfma_i32_16x16x64_i8 v[18:21], v[180:183], v[210:213], v[18:21]
	v_mfma_i32_16x16x64_i8 v[6:9], v[172:175], v[218:221], v[6:9]
	v_mfma_i32_16x16x64_i8 v[2:5], v[180:183], v[218:221], v[2:5]
	s_setprio 0
	s_barrier
	s_add_i32 s62, s62, 2
	s_add_u32 s46, s46, 0x100
	s_addc_u32 s47, s47, 0
	s_add_u32 s58, s58, 0x100
	s_addc_u32 s59, s59, 0
	s_cmp_gt_u32 s62, 13
	s_cbranch_scc0 .LBB0_1112
	s_and_b64 vcc, exec, s[12:13]
	s_cbranch_vccz .LBB0_1115
	s_barrier
